# v69 + loop-carried SALU block hoisted above the loop-back barrier in the six GEMM K-loops
# speedup vs baseline: 1.0064x; 1.0005x over previous
; #define PG8_STAGE(bufoff, gbase, voff) do { _Pragma("unroll") for (int _i = 0; _i < 2; ++_i) \
;         __builtin_amdgcn_global_load_lds((const unsigned*)((const char*)(gbase) + (voff)[_i]), (LAS unsigned*)(lds + (bufoff) + ldsw + _i * 8192), 16, 0, 0); } while (0)
; #define PG8_LDA(dst, b, h) do { if constexpr (FP8) { _Pragma("unroll") for (int m = 0; m < 4; ++m) dst##8[m] = PG8_LD8(lds + PG8_SA(b, h) + aoff + m * 2048); } \
;         else { _Pragma("unroll") for (int m = 0; m < 4; ++m) _Pragma("unroll") for (int k = 0; k < 2; ++k) dst[m][k] = *(const LAS bf16x8*)(lds + PG8_SA(b, h) + aoff + m * 2048 + k * 1024); } } while (0)
; #define PG8_WAIT_V(n) asm volatile("s_waitcnt vmcnt(" #n ")" ::: "memory")
; #define PG8_WAIT_L(n) asm volatile("s_waitcnt lgkmcnt(" #n ")" ::: "memory")
; template <class Epi, class Sched, bool GATHER, bool FP8 = false>
; __device__ __forceinline__ void gemm_phase(LAS unsigned char* lds, const Gemm g, const Sched& S, const Epi& E) {
;     ...
;         for (int t = 0; t < nt; t += 2) {
;             const bool last = (t == nt - 2);
;             const char* a1 = cA + (size_t)(t + 1) * kstep;
;             const char* a2 = last ? nA : cA + (size_t)(t + 2) * kstep; const char* b2 = last ? nB : cB + (size_t)(t + 2) * kstep;
;             const char* a3 = a2 + kstep; const char* b3 = b2 + kstep;
;             PG8_LDB(B0, 0, 0); PG8_LDB(B1, 0, 1); PG8_SCHED; PG8_LDA(At, 0, 0); PG8_STAGE_A(PG8_SA(1, 1), a1, 1, false);
;             PG8_WAIT_V(8); PG8_WAIT_L(0); PG8_BAR; PG8_MMA(0, 0, At, B0); PG8_MMA(0, 1, At, B1); PG8_BAR; PG8_SCHED;
;             PG8_LDA(At, 0, 1); PG8_STAGE(PG8_SB(0, 0), b2, voffB); PG8_STAGE(PG8_SB(0, 1), b2 + hstep, voffB); PG8_STAGE_A(PG8_SA(0, 0), a2, 0, last);
;             PG8_WAIT_V(8); PG8_WAIT_L(0); PG8_BAR; PG8_MMA(1, 0, At, B0); PG8_MMA(1, 1, At, B1); PG8_BAR; PG8_SCHED;
;             PG8_LDB(B0, 1, 0); PG8_LDB(B1, 1, 1); PG8_SCHED; PG8_LDA(At, 1, 0); PG8_STAGE_A(PG8_SA(0, 1), a2, 1, last);
;             PG8_WAIT_V(8); PG8_WAIT_L(0); PG8_BAR; PG8_MMA(0, 0, At, B0); PG8_MMA(0, 1, At, B1); PG8_BAR; PG8_SCHED;
;             PG8_LDA(At, 1, 1); PG8_STAGE(PG8_SB(1, 0), b3, voffB); PG8_STAGE(PG8_SB(1, 1), b3 + hstep, voffB); PG8_STAGE_A(PG8_SA(1, 0), a3, 0, last);
;             PG8_WAIT_V(8); PG8_WAIT_L(0); PG8_BAR; PG8_MMA(1, 0, At, B0); PG8_MMA(1, 1, At, B1); PG8_BAR; PG8_SCHED;
.LBB0_140:
	ds_read_b128 v[146:149], v152
	ds_read_b128 v[156:159], v152 offset:1024
	ds_read_b128 v[160:163], v152 offset:2048
	ds_read_b128 v[164:167], v152 offset:3072
	ds_read_b128 v[172:175], v153
	ds_read_b128 v[176:179], v153 offset:1024
	ds_read_b128 v[180:183], v153 offset:2048
	ds_read_b128 v[184:187], v153 offset:3072
	s_add_u32 s22, s20, 0xfff80080
	s_addc_u32 s23, s21, -1
	s_cmp_eq_u32 s48, 28
	s_cselect_b32 s25, s13, s23
	s_cselect_b32 s24, s44, s22
	s_cselect_b32 s23, s11, s47
	s_cselect_b32 s22, s45, s46
	v_lshl_add_u64 v[168:169], s[20:21], 0, v[138:139]
	s_add_i32 m0, s19, 0xc000
	ds_read_b128 v[188:191], v154
	ds_read_b128 v[192:195], v154 offset:1024
	ds_read_b128 v[196:199], v154 offset:2048
	ds_read_b128 v[200:203], v154 offset:3072
	ds_read_b128 v[204:207], v154 offset:4096
	ds_read_b128 v[208:211], v154 offset:5120
	ds_read_b128 v[212:215], v154 offset:6144
	ds_read_b128 v[216:219], v154 offset:7168
	global_load_lds_dwordx4 v[168:169], off
	v_lshl_add_u64 v[168:169], s[20:21], 0, v[140:141]
	s_add_i32 m0, s19, 0xe000
	s_nop 0
	global_load_lds_dwordx4 v[168:169], off
	s_waitcnt vmcnt(8)
	s_waitcnt lgkmcnt(0)
	s_barrier
	s_setprio 1
	s_waitcnt lgkmcnt(0)
	v_mfma_f32_16x16x32_bf16 v[126:129], v[146:149], v[188:191], v[126:129]
	v_mfma_f32_16x16x32_bf16 v[122:125], v[160:163], v[188:191], v[122:125]
	v_mfma_f32_16x16x32_bf16 v[118:121], v[146:149], v[196:199], v[118:121]
	v_mfma_f32_16x16x32_bf16 v[110:113], v[160:163], v[196:199], v[110:113]
	v_mfma_f32_16x16x32_bf16 v[102:105], v[146:149], v[204:207], v[102:105]
	v_mfma_f32_16x16x32_bf16 v[94:97], v[160:163], v[204:207], v[94:97]
	v_mfma_f32_16x16x32_bf16 v[86:89], v[146:149], v[212:215], v[86:89]
	v_mfma_f32_16x16x32_bf16 v[78:81], v[160:163], v[212:215], v[78:81]
	v_mfma_f32_16x16x32_bf16 v[126:129], v[156:159], v[192:195], v[126:129]
	v_mfma_f32_16x16x32_bf16 v[122:125], v[164:167], v[192:195], v[122:125]
	v_mfma_f32_16x16x32_bf16 v[118:121], v[156:159], v[200:203], v[118:121]
	v_mfma_f32_16x16x32_bf16 v[110:113], v[164:167], v[200:203], v[110:113]
	v_mfma_f32_16x16x32_bf16 v[102:105], v[156:159], v[208:211], v[102:105]
	v_mfma_f32_16x16x32_bf16 v[94:97], v[164:167], v[208:211], v[94:97]
	v_mfma_f32_16x16x32_bf16 v[86:89], v[156:159], v[216:219], v[86:89]
	v_mfma_f32_16x16x32_bf16 v[78:81], v[164:167], v[216:219], v[78:81]
	s_setprio 0
	s_setprio 1
	v_mfma_f32_16x16x32_bf16 v[114:117], v[172:175], v[188:191], v[114:117]
	v_mfma_f32_16x16x32_bf16 v[106:109], v[180:183], v[188:191], v[106:109]
	v_mfma_f32_16x16x32_bf16 v[98:101], v[172:175], v[196:199], v[98:101]
	v_mfma_f32_16x16x32_bf16 v[90:93], v[180:183], v[196:199], v[90:93]
	v_mfma_f32_16x16x32_bf16 v[82:85], v[172:175], v[204:207], v[82:85]
	v_mfma_f32_16x16x32_bf16 v[74:77], v[180:183], v[204:207], v[74:77]
	v_mfma_f32_16x16x32_bf16 v[70:73], v[172:175], v[212:215], v[70:73]
	v_mfma_f32_16x16x32_bf16 v[66:69], v[180:183], v[212:215], v[66:69]
	v_mfma_f32_16x16x32_bf16 v[114:117], v[176:179], v[192:195], v[114:117]
	v_mfma_f32_16x16x32_bf16 v[106:109], v[184:187], v[192:195], v[106:109]
	v_mfma_f32_16x16x32_bf16 v[98:101], v[176:179], v[200:203], v[98:101]
	v_mfma_f32_16x16x32_bf16 v[90:93], v[184:187], v[200:203], v[90:93]
	v_mfma_f32_16x16x32_bf16 v[82:85], v[176:179], v[208:211], v[82:85]
	v_mfma_f32_16x16x32_bf16 v[74:77], v[184:187], v[208:211], v[74:77]
	v_mfma_f32_16x16x32_bf16 v[70:73], v[176:179], v[216:219], v[70:73]
	v_mfma_f32_16x16x32_bf16 v[66:69], v[184:187], v[216:219], v[66:69]
	s_setprio 0
	s_barrier
	s_add_i32 s49, s40, s31
	v_lshl_add_u64 v[168:169], s[22:23], 0, v[132:133]
	s_mov_b32 m0, s49
	ds_read_b128 v[188:191], v154 offset:16384
	ds_read_b128 v[192:195], v154 offset:17408
	ds_read_b128 v[196:199], v154 offset:18432
	ds_read_b128 v[200:203], v154 offset:19456
	ds_read_b128 v[204:207], v154 offset:20480
	ds_read_b128 v[208:211], v154 offset:21504
	ds_read_b128 v[212:215], v154 offset:22528
	ds_read_b128 v[216:219], v154 offset:23552
	global_load_lds_dwordx4 v[168:169], off
	s_add_i32 m0, s49, 0x2000
	s_add_u32 s50, s22, 0x80000
	v_lshl_add_u64 v[220:221], s[22:23], 0, v[136:137]
	s_addc_u32 s51, s23, 0
	s_add_i32 s49, s41, s31
	global_load_lds_dwordx4 v[220:221], off
	v_lshl_add_u64 v[222:223], s[50:51], 0, v[132:133]
	s_mov_b32 m0, s49
	v_lshl_add_u64 v[224:225], s[24:25], 0, v[134:135]
	global_load_lds_dwordx4 v[222:223], off
	v_lshl_add_u64 v[222:223], s[50:51], 0, v[136:137]
	s_add_i32 m0, s49, 0x2000
	s_nop 0
	global_load_lds_dwordx4 v[222:223], off
	v_lshl_add_u64 v[222:223], s[24:25], 0, v[130:131]
	s_mov_b32 m0, s19
	s_nop 0
	global_load_lds_dwordx4 v[222:223], off
	s_mov_b32 m0, s33
	s_nop 0
	global_load_lds_dwordx4 v[224:225], off
	s_waitcnt vmcnt(8)
	s_waitcnt lgkmcnt(0)
	s_barrier
; #define PG8_STAGE(bufoff, gbase, voff) do { _Pragma("unroll") for (int _i = 0; _i < 2; ++_i) \
;         __builtin_amdgcn_global_load_lds((const unsigned*)((const char*)(gbase) + (voff)[_i]), (LAS unsigned*)(lds + (bufoff) + ldsw + _i * 8192), 16, 0, 0); } while (0)
; #define PG8_LDA(dst, b, h) do { if constexpr (FP8) { _Pragma("unroll") for (int m = 0; m < 4; ++m) dst##8[m] = PG8_LD8(lds + PG8_SA(b, h) + aoff + m * 2048); } \
;         else { _Pragma("unroll") for (int m = 0; m < 4; ++m) _Pragma("unroll") for (int k = 0; k < 2; ++k) dst[m][k] = *(const LAS bf16x8*)(lds + PG8_SA(b, h) + aoff + m * 2048 + k * 1024); } } while (0)
; #define PG8_WAIT_V(n) asm volatile("s_waitcnt vmcnt(" #n ")" ::: "memory")
; #define PG8_WAIT_L(n) asm volatile("s_waitcnt lgkmcnt(" #n ")" ::: "memory")
; template <class Epi, class Sched, bool GATHER, bool FP8 = false>
; __device__ __forceinline__ void gemm_phase(LAS unsigned char* lds, const Gemm g, const Sched& S, const Epi& E) {
;     ...
;         for (int t = 0; t < nt; t += 2) {
;             const bool last = (t == nt - 2);
;             const char* a1 = cA + (size_t)(t + 1) * kstep;
;             const char* a2 = last ? nA : cA + (size_t)(t + 2) * kstep; const char* b2 = last ? nB : cB + (size_t)(t + 2) * kstep;
;             const char* a3 = a2 + kstep; const char* b3 = b2 + kstep;
;             PG8_LDB(B0, 0, 0); PG8_LDB(B1, 0, 1); PG8_SCHED; PG8_LDA(At, 0, 0); PG8_STAGE_A(PG8_SA(1, 1), a1, 1, false);
;             PG8_WAIT_V(8); PG8_WAIT_L(0); PG8_BAR; PG8_MMA(0, 0, At, B0); PG8_MMA(0, 1, At, B1); PG8_BAR; PG8_SCHED;
;             PG8_LDA(At, 0, 1); PG8_STAGE(PG8_SB(0, 0), b2, voffB); PG8_STAGE(PG8_SB(0, 1), b2 + hstep, voffB); PG8_STAGE_A(PG8_SA(0, 0), a2, 0, last);
;             PG8_WAIT_V(8); PG8_WAIT_L(0); PG8_BAR; PG8_MMA(1, 0, At, B0); PG8_MMA(1, 1, At, B1); PG8_BAR; PG8_SCHED;
;             PG8_LDB(B0, 1, 0); PG8_LDB(B1, 1, 1); PG8_SCHED; PG8_LDA(At, 1, 0); PG8_STAGE_A(PG8_SA(0, 1), a2, 1, last);
;             PG8_WAIT_V(8); PG8_WAIT_L(0); PG8_BAR; PG8_MMA(0, 0, At, B0); PG8_MMA(0, 1, At, B1); PG8_BAR; PG8_SCHED;
;             PG8_LDA(At, 1, 1); PG8_STAGE(PG8_SB(1, 0), b3, voffB); PG8_STAGE(PG8_SB(1, 1), b3 + hstep, voffB); PG8_STAGE_A(PG8_SA(1, 0), a3, 0, last);
;             PG8_WAIT_V(8); PG8_WAIT_L(0); PG8_BAR; PG8_MMA(1, 0, At, B0); PG8_MMA(1, 1, At, B1); PG8_BAR; PG8_SCHED;
	s_setprio 1
	s_waitcnt lgkmcnt(0)
	v_mfma_f32_16x16x32_bf16 v[62:65], v[146:149], v[188:191], v[62:65]
	v_mfma_f32_16x16x32_bf16 v[58:61], v[160:163], v[188:191], v[58:61]
	v_mfma_f32_16x16x32_bf16 v[54:57], v[146:149], v[196:199], v[54:57]
	v_mfma_f32_16x16x32_bf16 v[46:49], v[160:163], v[196:199], v[46:49]
	v_mfma_f32_16x16x32_bf16 v[38:41], v[146:149], v[204:207], v[38:41]
	v_mfma_f32_16x16x32_bf16 v[30:33], v[160:163], v[204:207], v[30:33]
	v_mfma_f32_16x16x32_bf16 v[22:25], v[146:149], v[212:215], v[22:25]
	v_mfma_f32_16x16x32_bf16 v[14:17], v[160:163], v[212:215], v[14:17]
	v_mfma_f32_16x16x32_bf16 v[62:65], v[156:159], v[192:195], v[62:65]
	v_mfma_f32_16x16x32_bf16 v[58:61], v[164:167], v[192:195], v[58:61]
	v_mfma_f32_16x16x32_bf16 v[54:57], v[156:159], v[200:203], v[54:57]
	v_mfma_f32_16x16x32_bf16 v[46:49], v[164:167], v[200:203], v[46:49]
	v_mfma_f32_16x16x32_bf16 v[38:41], v[156:159], v[208:211], v[38:41]
	v_mfma_f32_16x16x32_bf16 v[30:33], v[164:167], v[208:211], v[30:33]
	v_mfma_f32_16x16x32_bf16 v[22:25], v[156:159], v[216:219], v[22:25]
	v_mfma_f32_16x16x32_bf16 v[14:17], v[164:167], v[216:219], v[14:17]
	s_setprio 0
	s_setprio 1
	v_mfma_f32_16x16x32_bf16 v[50:53], v[172:175], v[188:191], v[50:53]
	v_mfma_f32_16x16x32_bf16 v[42:45], v[180:183], v[188:191], v[42:45]
	v_mfma_f32_16x16x32_bf16 v[34:37], v[172:175], v[196:199], v[34:37]
	v_mfma_f32_16x16x32_bf16 v[26:29], v[180:183], v[196:199], v[26:29]
	v_mfma_f32_16x16x32_bf16 v[18:21], v[172:175], v[204:207], v[18:21]
	v_mfma_f32_16x16x32_bf16 v[10:13], v[180:183], v[204:207], v[10:13]
	v_mfma_f32_16x16x32_bf16 v[6:9], v[172:175], v[212:215], v[6:9]
	v_mfma_f32_16x16x32_bf16 v[2:5], v[180:183], v[212:215], v[2:5]
	v_mfma_f32_16x16x32_bf16 v[50:53], v[176:179], v[192:195], v[50:53]
	v_mfma_f32_16x16x32_bf16 v[42:45], v[184:187], v[192:195], v[42:45]
	v_mfma_f32_16x16x32_bf16 v[34:37], v[176:179], v[200:203], v[34:37]
	v_mfma_f32_16x16x32_bf16 v[26:29], v[184:187], v[200:203], v[26:29]
	v_mfma_f32_16x16x32_bf16 v[18:21], v[176:179], v[208:211], v[18:21]
	v_mfma_f32_16x16x32_bf16 v[10:13], v[184:187], v[208:211], v[10:13]
	v_mfma_f32_16x16x32_bf16 v[6:9], v[176:179], v[216:219], v[6:9]
	v_mfma_f32_16x16x32_bf16 v[2:5], v[184:187], v[216:219], v[2:5]
	s_setprio 0
	s_barrier
	s_add_i32 s49, 0, 0x18000
	v_add_u32_e32 v155, s49, v150
	s_add_i32 s50, 0, 0x1c000
	ds_read_b128 v[146:149], v155
	ds_read_b128 v[156:159], v155 offset:1024
	ds_read_b128 v[160:163], v155 offset:2048
	ds_read_b128 v[164:167], v155 offset:3072
	v_add_u32_e32 v155, s50, v150
	ds_read_b128 v[172:175], v155
	ds_read_b128 v[176:179], v155 offset:1024
	ds_read_b128 v[180:183], v155 offset:2048
	ds_read_b128 v[184:187], v155 offset:3072
	s_add_u32 s24, s24, 0x80000
	s_addc_u32 s25, s25, 0
	s_mov_b32 m0, s34
	v_lshl_add_u64 v[226:227], s[24:25], 0, v[130:131]
	ds_read_b128 v[188:191], v154 offset:32768
	ds_read_b128 v[192:195], v154 offset:33792
	ds_read_b128 v[196:199], v154 offset:34816
	ds_read_b128 v[200:203], v154 offset:35840
	ds_read_b128 v[204:207], v154 offset:36864
	ds_read_b128 v[208:211], v154 offset:37888
	ds_read_b128 v[212:215], v154 offset:38912
	ds_read_b128 v[216:219], v154 offset:39936
	global_load_lds_dwordx4 v[226:227], off
	v_lshl_add_u64 v[226:227], s[24:25], 0, v[134:135]
	s_mov_b32 m0, s35
	s_nop 0
	global_load_lds_dwordx4 v[226:227], off
	s_waitcnt vmcnt(8)
	s_waitcnt lgkmcnt(0)
	s_barrier
	s_setprio 1
	s_waitcnt lgkmcnt(0)
	v_mfma_f32_16x16x32_bf16 v[126:129], v[146:149], v[188:191], v[126:129]
	v_mfma_f32_16x16x32_bf16 v[122:125], v[160:163], v[188:191], v[122:125]
	v_mfma_f32_16x16x32_bf16 v[118:121], v[146:149], v[196:199], v[118:121]
	v_mfma_f32_16x16x32_bf16 v[110:113], v[160:163], v[196:199], v[110:113]
	v_mfma_f32_16x16x32_bf16 v[102:105], v[146:149], v[204:207], v[102:105]
	v_mfma_f32_16x16x32_bf16 v[94:97], v[160:163], v[204:207], v[94:97]
	v_mfma_f32_16x16x32_bf16 v[86:89], v[146:149], v[212:215], v[86:89]
	v_mfma_f32_16x16x32_bf16 v[78:81], v[160:163], v[212:215], v[78:81]
	v_mfma_f32_16x16x32_bf16 v[126:129], v[156:159], v[192:195], v[126:129]
	v_mfma_f32_16x16x32_bf16 v[122:125], v[164:167], v[192:195], v[122:125]
	v_mfma_f32_16x16x32_bf16 v[118:121], v[156:159], v[200:203], v[118:121]
	v_mfma_f32_16x16x32_bf16 v[110:113], v[164:167], v[200:203], v[110:113]
	v_mfma_f32_16x16x32_bf16 v[102:105], v[156:159], v[208:211], v[102:105]
	v_mfma_f32_16x16x32_bf16 v[94:97], v[164:167], v[208:211], v[94:97]
	v_mfma_f32_16x16x32_bf16 v[86:89], v[156:159], v[216:219], v[86:89]
	v_mfma_f32_16x16x32_bf16 v[78:81], v[164:167], v[216:219], v[78:81]
	s_setprio 0
	s_setprio 1
	v_mfma_f32_16x16x32_bf16 v[114:117], v[172:175], v[188:191], v[114:117]
	v_mfma_f32_16x16x32_bf16 v[106:109], v[180:183], v[188:191], v[106:109]
	v_mfma_f32_16x16x32_bf16 v[98:101], v[172:175], v[196:199], v[98:101]
	v_mfma_f32_16x16x32_bf16 v[90:93], v[180:183], v[196:199], v[90:93]
	v_mfma_f32_16x16x32_bf16 v[82:85], v[172:175], v[204:207], v[82:85]
	v_mfma_f32_16x16x32_bf16 v[74:77], v[180:183], v[204:207], v[74:77]
	v_mfma_f32_16x16x32_bf16 v[70:73], v[172:175], v[212:215], v[70:73]
	v_mfma_f32_16x16x32_bf16 v[66:69], v[180:183], v[212:215], v[66:69]
	v_mfma_f32_16x16x32_bf16 v[114:117], v[176:179], v[192:195], v[114:117]
	v_mfma_f32_16x16x32_bf16 v[106:109], v[184:187], v[192:195], v[106:109]
	v_mfma_f32_16x16x32_bf16 v[98:101], v[176:179], v[200:203], v[98:101]
	v_mfma_f32_16x16x32_bf16 v[90:93], v[184:187], v[200:203], v[90:93]
	v_mfma_f32_16x16x32_bf16 v[82:85], v[176:179], v[208:211], v[82:85]
	v_mfma_f32_16x16x32_bf16 v[74:77], v[184:187], v[208:211], v[74:77]
	v_mfma_f32_16x16x32_bf16 v[70:73], v[176:179], v[216:219], v[70:73]
	v_mfma_f32_16x16x32_bf16 v[66:69], v[184:187], v[216:219], v[66:69]
	s_setprio 0
	s_barrier
; #define PG8_STAGE(bufoff, gbase, voff) do { _Pragma("unroll") for (int _i = 0; _i < 2; ++_i) \
;         __builtin_amdgcn_global_load_lds((const unsigned*)((const char*)(gbase) + (voff)[_i]), (LAS unsigned*)(lds + (bufoff) + ldsw + _i * 8192), 16, 0, 0); } while (0)
; #define PG8_LDA(dst, b, h) do { if constexpr (FP8) { _Pragma("unroll") for (int m = 0; m < 4; ++m) dst##8[m] = PG8_LD8(lds + PG8_SA(b, h) + aoff + m * 2048); } \
;         else { _Pragma("unroll") for (int m = 0; m < 4; ++m) _Pragma("unroll") for (int k = 0; k < 2; ++k) dst[m][k] = *(const LAS bf16x8*)(lds + PG8_SA(b, h) + aoff + m * 2048 + k * 1024); } } while (0)
; #define PG8_WAIT_V(n) asm volatile("s_waitcnt vmcnt(" #n ")" ::: "memory")
; #define PG8_WAIT_L(n) asm volatile("s_waitcnt lgkmcnt(" #n ")" ::: "memory")
; template <class Epi, class Sched, bool GATHER, bool FP8 = false>
; __device__ __forceinline__ void gemm_phase(LAS unsigned char* lds, const Gemm g, const Sched& S, const Epi& E) {
;     ...
;         for (int t = 0; t < nt; t += 2) {
;             const bool last = (t == nt - 2);
;             const char* a1 = cA + (size_t)(t + 1) * kstep;
;             const char* a2 = last ? nA : cA + (size_t)(t + 2) * kstep; const char* b2 = last ? nB : cB + (size_t)(t + 2) * kstep;
;             const char* a3 = a2 + kstep; const char* b3 = b2 + kstep;
;             PG8_LDB(B0, 0, 0); PG8_LDB(B1, 0, 1); PG8_SCHED; PG8_LDA(At, 0, 0); PG8_STAGE_A(PG8_SA(1, 1), a1, 1, false);
;             PG8_WAIT_V(8); PG8_WAIT_L(0); PG8_BAR; PG8_MMA(0, 0, At, B0); PG8_MMA(0, 1, At, B1); PG8_BAR; PG8_SCHED;
;             PG8_LDA(At, 0, 1); PG8_STAGE(PG8_SB(0, 0), b2, voffB); PG8_STAGE(PG8_SB(0, 1), b2 + hstep, voffB); PG8_STAGE_A(PG8_SA(0, 0), a2, 0, last);
;             PG8_WAIT_V(8); PG8_WAIT_L(0); PG8_BAR; PG8_MMA(1, 0, At, B0); PG8_MMA(1, 1, At, B1); PG8_BAR; PG8_SCHED;
;             PG8_LDB(B0, 1, 0); PG8_LDB(B1, 1, 1); PG8_SCHED; PG8_LDA(At, 1, 0); PG8_STAGE_A(PG8_SA(0, 1), a2, 1, last);
;             PG8_WAIT_V(8); PG8_WAIT_L(0); PG8_BAR; PG8_MMA(0, 0, At, B0); PG8_MMA(0, 1, At, B1); PG8_BAR; PG8_SCHED;
;             PG8_LDA(At, 1, 1); PG8_STAGE(PG8_SB(1, 0), b3, voffB); PG8_STAGE(PG8_SB(1, 1), b3 + hstep, voffB); PG8_STAGE_A(PG8_SA(1, 0), a3, 0, last);
;             PG8_WAIT_V(8); PG8_WAIT_L(0); PG8_BAR; PG8_MMA(1, 0, At, B0); PG8_MMA(1, 1, At, B1); PG8_BAR; PG8_SCHED;
	s_add_i32 s24, s49, s31
	v_lshl_add_u64 v[168:169], v[168:169], 0, s[6:7]
	s_mov_b32 m0, s24
	ds_read_b128 v[188:191], v154 offset:49152
	ds_read_b128 v[192:195], v154 offset:50176
	ds_read_b128 v[196:199], v154 offset:51200
	ds_read_b128 v[200:203], v154 offset:52224
	ds_read_b128 v[204:207], v154 offset:53248
	ds_read_b128 v[208:211], v154 offset:54272
	ds_read_b128 v[212:215], v154 offset:55296
	ds_read_b128 v[216:219], v154 offset:56320
	global_load_lds_dwordx4 v[168:169], off
	s_add_i32 m0, s24, 0x2000
	s_add_u32 s22, s22, 0x80080
	v_lshl_add_u64 v[168:169], v[220:221], 0, s[6:7]
	s_addc_u32 s23, s23, 0
	s_add_i32 s24, s50, s31
	global_load_lds_dwordx4 v[168:169], off
	v_lshl_add_u64 v[168:169], s[22:23], 0, v[132:133]
	s_mov_b32 m0, s24
	s_nop 0
	global_load_lds_dwordx4 v[168:169], off
	v_lshl_add_u64 v[168:169], s[22:23], 0, v[136:137]
	s_add_i32 m0, s24, 0x2000
	s_nop 0
	global_load_lds_dwordx4 v[168:169], off
	v_lshl_add_u64 v[168:169], v[222:223], 0, s[6:7]
	s_mov_b32 m0, s37
	s_nop 0
	global_load_lds_dwordx4 v[168:169], off
	v_lshl_add_u64 v[168:169], v[224:225], 0, s[6:7]
	s_mov_b32 m0, s38
	s_nop 0
	global_load_lds_dwordx4 v[168:169], off
	s_waitcnt vmcnt(8)
	s_waitcnt lgkmcnt(0)
	s_barrier
	s_setprio 1
	s_waitcnt lgkmcnt(0)
	v_mfma_f32_16x16x32_bf16 v[62:65], v[146:149], v[188:191], v[62:65]
	v_mfma_f32_16x16x32_bf16 v[58:61], v[160:163], v[188:191], v[58:61]
	v_mfma_f32_16x16x32_bf16 v[54:57], v[146:149], v[196:199], v[54:57]
	v_mfma_f32_16x16x32_bf16 v[46:49], v[160:163], v[196:199], v[46:49]
	v_mfma_f32_16x16x32_bf16 v[38:41], v[146:149], v[204:207], v[38:41]
	v_mfma_f32_16x16x32_bf16 v[30:33], v[160:163], v[204:207], v[30:33]
	v_mfma_f32_16x16x32_bf16 v[22:25], v[146:149], v[212:215], v[22:25]
	v_mfma_f32_16x16x32_bf16 v[14:17], v[160:163], v[212:215], v[14:17]
	v_mfma_f32_16x16x32_bf16 v[62:65], v[156:159], v[192:195], v[62:65]
	v_mfma_f32_16x16x32_bf16 v[58:61], v[164:167], v[192:195], v[58:61]
	v_mfma_f32_16x16x32_bf16 v[54:57], v[156:159], v[200:203], v[54:57]
	v_mfma_f32_16x16x32_bf16 v[46:49], v[164:167], v[200:203], v[46:49]
	v_mfma_f32_16x16x32_bf16 v[38:41], v[156:159], v[208:211], v[38:41]
	v_mfma_f32_16x16x32_bf16 v[30:33], v[164:167], v[208:211], v[30:33]
	v_mfma_f32_16x16x32_bf16 v[22:25], v[156:159], v[216:219], v[22:25]
	v_mfma_f32_16x16x32_bf16 v[14:17], v[164:167], v[216:219], v[14:17]
	s_setprio 0
	s_setprio 1
	v_mfma_f32_16x16x32_bf16 v[50:53], v[172:175], v[188:191], v[50:53]
	v_mfma_f32_16x16x32_bf16 v[42:45], v[180:183], v[188:191], v[42:45]
	v_mfma_f32_16x16x32_bf16 v[34:37], v[172:175], v[196:199], v[34:37]
	v_mfma_f32_16x16x32_bf16 v[26:29], v[180:183], v[196:199], v[26:29]
	v_mfma_f32_16x16x32_bf16 v[18:21], v[172:175], v[204:207], v[18:21]
	v_mfma_f32_16x16x32_bf16 v[10:13], v[180:183], v[204:207], v[10:13]
	v_mfma_f32_16x16x32_bf16 v[6:9], v[172:175], v[212:215], v[6:9]
	v_mfma_f32_16x16x32_bf16 v[2:5], v[180:183], v[212:215], v[2:5]
	v_mfma_f32_16x16x32_bf16 v[50:53], v[176:179], v[192:195], v[50:53]
	v_mfma_f32_16x16x32_bf16 v[42:45], v[184:187], v[192:195], v[42:45]
	v_mfma_f32_16x16x32_bf16 v[34:37], v[176:179], v[200:203], v[34:37]
	v_mfma_f32_16x16x32_bf16 v[26:29], v[184:187], v[200:203], v[26:29]
	v_mfma_f32_16x16x32_bf16 v[18:21], v[176:179], v[208:211], v[18:21]
	v_mfma_f32_16x16x32_bf16 v[10:13], v[184:187], v[208:211], v[10:13]
	v_mfma_f32_16x16x32_bf16 v[6:9], v[176:179], v[216:219], v[6:9]
	v_mfma_f32_16x16x32_bf16 v[2:5], v[184:187], v[216:219], v[2:5]
	s_setprio 0
	s_add_i32 s48, s48, 2
	s_add_u32 s20, s20, 0x100
	s_addc_u32 s21, s21, 0
	s_add_u32 s46, s46, 0x100
	s_addc_u32 s47, s47, 0
	s_cmp_gt_u32 s48, 29
	s_barrier
	s_cbranch_scc0 .LBB0_140
	s_and_b64 vcc, exec, s[8:9]
	s_cbranch_vccz .LBB0_143
	s_barrier

; #define PG8_STAGE(bufoff, gbase, voff) do { _Pragma("unroll") for (int _i = 0; _i < 2; ++_i) \
;         __builtin_amdgcn_global_load_lds((const unsigned*)((const char*)(gbase) + (voff)[_i]), (LAS unsigned*)(lds + (bufoff) + ldsw + _i * 8192), 16, 0, 0); } while (0)
; #define PG8_LDA(dst, b, h) do { if constexpr (FP8) { _Pragma("unroll") for (int m = 0; m < 4; ++m) dst##8[m] = PG8_LD8(lds + PG8_SA(b, h) + aoff + m * 2048); } \
;         else { _Pragma("unroll") for (int m = 0; m < 4; ++m) _Pragma("unroll") for (int k = 0; k < 2; ++k) dst[m][k] = *(const LAS bf16x8*)(lds + PG8_SA(b, h) + aoff + m * 2048 + k * 1024); } } while (0)
; #define PG8_WAIT_V(n) asm volatile("s_waitcnt vmcnt(" #n ")" ::: "memory")
; #define PG8_WAIT_L(n) asm volatile("s_waitcnt lgkmcnt(" #n ")" ::: "memory")
; template <class Epi, class Sched, bool GATHER, bool FP8 = false>
; __device__ __forceinline__ void gemm_phase(LAS unsigned char* lds, const Gemm g, const Sched& S, const Epi& E) {
;     ...
;         for (int t = 0; t < nt; t += 2) {
;             const bool last = (t == nt - 2);
;             const char* a1 = cA + (size_t)(t + 1) * kstep;
;             const char* a2 = last ? nA : cA + (size_t)(t + 2) * kstep; const char* b2 = last ? nB : cB + (size_t)(t + 2) * kstep;
;             const char* a3 = a2 + kstep; const char* b3 = b2 + kstep;
;             PG8_LDB(B0, 0, 0); PG8_LDB(B1, 0, 1); PG8_SCHED; PG8_LDA(At, 0, 0); PG8_STAGE_A(PG8_SA(1, 1), a1, 1, false);
;             PG8_WAIT_V(8); PG8_WAIT_L(0); PG8_BAR; PG8_MMA(0, 0, At, B0); PG8_MMA(0, 1, At, B1); PG8_BAR; PG8_SCHED;
;             PG8_LDA(At, 0, 1); PG8_STAGE(PG8_SB(0, 0), b2, voffB); PG8_STAGE(PG8_SB(0, 1), b2 + hstep, voffB); PG8_STAGE_A(PG8_SA(0, 0), a2, 0, last);
;             PG8_WAIT_V(8); PG8_WAIT_L(0); PG8_BAR; PG8_MMA(1, 0, At, B0); PG8_MMA(1, 1, At, B1); PG8_BAR; PG8_SCHED;
;             PG8_LDB(B0, 1, 0); PG8_LDB(B1, 1, 1); PG8_SCHED; PG8_LDA(At, 1, 0); PG8_STAGE_A(PG8_SA(0, 1), a2, 1, last);
;             PG8_WAIT_V(8); PG8_WAIT_L(0); PG8_BAR; PG8_MMA(0, 0, At, B0); PG8_MMA(0, 1, At, B1); PG8_BAR; PG8_SCHED;
;             PG8_LDA(At, 1, 1); PG8_STAGE(PG8_SB(1, 0), b3, voffB); PG8_STAGE(PG8_SB(1, 1), b3 + hstep, voffB); PG8_STAGE_A(PG8_SA(1, 0), a3, 0, last);
;             PG8_WAIT_V(8); PG8_WAIT_L(0); PG8_BAR; PG8_MMA(1, 0, At, B0); PG8_MMA(1, 1, At, B1); PG8_BAR; PG8_SCHED;
.LBB0_279:
	ds_read_b128 v[150:153], v165
	ds_read_b128 v[172:175], v165 offset:1024
	ds_read_b128 v[176:179], v165 offset:2048
	ds_read_b128 v[180:183], v165 offset:3072
	ds_read_b128 v[184:187], v166
	ds_read_b128 v[188:191], v166 offset:1024
	ds_read_b128 v[192:195], v166 offset:2048
	ds_read_b128 v[196:199], v166 offset:3072
	s_add_u32 s28, s26, 0xfffe0080
	s_addc_u32 s29, s27, -1
	s_cmp_eq_u32 s55, 4
	s_cselect_b32 s31, s17, s29
	s_cselect_b32 s30, s23, s28
	s_cselect_b32 s29, s15, s54
	s_cselect_b32 s28, s52, s53
	v_lshl_add_u64 v[168:169], s[26:27], 0, v[142:143]
	s_add_i32 m0, s25, 0xc000
	ds_read_b128 v[200:203], v167
	ds_read_b128 v[204:207], v167 offset:1024
	ds_read_b128 v[208:211], v167 offset:2048
	ds_read_b128 v[212:215], v167 offset:3072
	ds_read_b128 v[216:219], v167 offset:4096
	ds_read_b128 v[220:223], v167 offset:5120
	ds_read_b128 v[224:227], v167 offset:6144
	ds_read_b128 v[228:231], v167 offset:7168
	global_load_lds_dwordx4 v[168:169], off
	v_lshl_add_u64 v[168:169], s[26:27], 0, v[144:145]
	s_add_i32 m0, s25, 0xe000
	s_nop 0
	global_load_lds_dwordx4 v[168:169], off
	s_waitcnt vmcnt(8)
	s_waitcnt lgkmcnt(0)
	s_barrier
	s_setprio 1
	s_waitcnt lgkmcnt(0)
	v_mfma_f32_16x16x32_bf16 v[126:129], v[150:153], v[200:203], v[126:129]
	v_mfma_f32_16x16x32_bf16 v[122:125], v[176:179], v[200:203], v[122:125]
	v_mfma_f32_16x16x32_bf16 v[118:121], v[150:153], v[208:211], v[118:121]
	v_mfma_f32_16x16x32_bf16 v[114:117], v[176:179], v[208:211], v[114:117]
	v_mfma_f32_16x16x32_bf16 v[110:113], v[150:153], v[216:219], v[110:113]
	v_mfma_f32_16x16x32_bf16 v[106:109], v[176:179], v[216:219], v[106:109]
	v_mfma_f32_16x16x32_bf16 v[102:105], v[150:153], v[224:227], v[102:105]
	v_mfma_f32_16x16x32_bf16 v[98:101], v[176:179], v[224:227], v[98:101]
	v_mfma_f32_16x16x32_bf16 v[126:129], v[172:175], v[204:207], v[126:129]
	v_mfma_f32_16x16x32_bf16 v[122:125], v[180:183], v[204:207], v[122:125]
	v_mfma_f32_16x16x32_bf16 v[118:121], v[172:175], v[212:215], v[118:121]
	v_mfma_f32_16x16x32_bf16 v[114:117], v[180:183], v[212:215], v[114:117]
	v_mfma_f32_16x16x32_bf16 v[110:113], v[172:175], v[220:223], v[110:113]
	v_mfma_f32_16x16x32_bf16 v[106:109], v[180:183], v[220:223], v[106:109]
	v_mfma_f32_16x16x32_bf16 v[102:105], v[172:175], v[228:231], v[102:105]
	v_mfma_f32_16x16x32_bf16 v[98:101], v[180:183], v[228:231], v[98:101]
	s_setprio 0
	s_setprio 1
	v_mfma_f32_16x16x32_bf16 v[62:65], v[184:187], v[200:203], v[62:65]
	v_mfma_f32_16x16x32_bf16 v[58:61], v[192:195], v[200:203], v[58:61]
	v_mfma_f32_16x16x32_bf16 v[54:57], v[184:187], v[208:211], v[54:57]
	v_mfma_f32_16x16x32_bf16 v[50:53], v[192:195], v[208:211], v[50:53]
	v_mfma_f32_16x16x32_bf16 v[46:49], v[184:187], v[216:219], v[46:49]
	v_mfma_f32_16x16x32_bf16 v[42:45], v[192:195], v[216:219], v[42:45]
	v_mfma_f32_16x16x32_bf16 v[38:41], v[184:187], v[224:227], v[38:41]
	v_mfma_f32_16x16x32_bf16 v[34:37], v[192:195], v[224:227], v[34:37]
	v_mfma_f32_16x16x32_bf16 v[62:65], v[188:191], v[204:207], v[62:65]
	v_mfma_f32_16x16x32_bf16 v[58:61], v[196:199], v[204:207], v[58:61]
	v_mfma_f32_16x16x32_bf16 v[54:57], v[188:191], v[212:215], v[54:57]
	v_mfma_f32_16x16x32_bf16 v[50:53], v[196:199], v[212:215], v[50:53]
	v_mfma_f32_16x16x32_bf16 v[46:49], v[188:191], v[220:223], v[46:49]
	v_mfma_f32_16x16x32_bf16 v[42:45], v[196:199], v[220:223], v[42:45]
	v_mfma_f32_16x16x32_bf16 v[38:41], v[188:191], v[228:231], v[38:41]
	v_mfma_f32_16x16x32_bf16 v[34:37], v[196:199], v[228:231], v[34:37]
	s_setprio 0
	s_barrier
	s_add_i32 s56, s46, s37
	v_lshl_add_u64 v[168:169], s[28:29], 0, v[134:135]
	s_mov_b32 m0, s56
	ds_read_b128 v[200:203], v167 offset:16384
	ds_read_b128 v[204:207], v167 offset:17408
	ds_read_b128 v[208:211], v167 offset:18432
	ds_read_b128 v[212:215], v167 offset:19456
	ds_read_b128 v[216:219], v167 offset:20480
	ds_read_b128 v[220:223], v167 offset:21504
	ds_read_b128 v[224:227], v167 offset:22528
	ds_read_b128 v[228:231], v167 offset:23552
	global_load_lds_dwordx4 v[168:169], off
	s_add_i32 m0, s56, 0x2000
	s_add_u32 s56, s28, 0x20000
	v_lshl_add_u64 v[232:233], s[28:29], 0, v[138:139]
	s_addc_u32 s57, s29, 0
	s_add_i32 s58, s47, s37
	global_load_lds_dwordx4 v[232:233], off
	v_lshl_add_u64 v[234:235], s[56:57], 0, v[134:135]
	s_mov_b32 m0, s58
	v_lshl_add_u64 v[236:237], s[30:31], 0, v[136:137]
	global_load_lds_dwordx4 v[234:235], off
	v_lshl_add_u64 v[234:235], s[56:57], 0, v[138:139]
	s_add_i32 m0, s58, 0x2000
	s_nop 0
	global_load_lds_dwordx4 v[234:235], off
	v_lshl_add_u64 v[234:235], s[30:31], 0, v[132:133]
	s_mov_b32 m0, s25
	s_nop 0
	global_load_lds_dwordx4 v[234:235], off
	s_mov_b32 m0, s38
	s_nop 0
	global_load_lds_dwordx4 v[236:237], off
	s_waitcnt vmcnt(8)
	s_waitcnt lgkmcnt(0)
	s_barrier
; #define PG8_STAGE(bufoff, gbase, voff) do { _Pragma("unroll") for (int _i = 0; _i < 2; ++_i) \
;         __builtin_amdgcn_global_load_lds((const unsigned*)((const char*)(gbase) + (voff)[_i]), (LAS unsigned*)(lds + (bufoff) + ldsw + _i * 8192), 16, 0, 0); } while (0)
; #define PG8_LDA(dst, b, h) do { if constexpr (FP8) { _Pragma("unroll") for (int m = 0; m < 4; ++m) dst##8[m] = PG8_LD8(lds + PG8_SA(b, h) + aoff + m * 2048); } \
;         else { _Pragma("unroll") for (int m = 0; m < 4; ++m) _Pragma("unroll") for (int k = 0; k < 2; ++k) dst[m][k] = *(const LAS bf16x8*)(lds + PG8_SA(b, h) + aoff + m * 2048 + k * 1024); } } while (0)
; #define PG8_WAIT_V(n) asm volatile("s_waitcnt vmcnt(" #n ")" ::: "memory")
; #define PG8_WAIT_L(n) asm volatile("s_waitcnt lgkmcnt(" #n ")" ::: "memory")
; template <class Epi, class Sched, bool GATHER, bool FP8 = false>
; __device__ __forceinline__ void gemm_phase(LAS unsigned char* lds, const Gemm g, const Sched& S, const Epi& E) {
;     ...
;         for (int t = 0; t < nt; t += 2) {
;             const bool last = (t == nt - 2);
;             const char* a1 = cA + (size_t)(t + 1) * kstep;
;             const char* a2 = last ? nA : cA + (size_t)(t + 2) * kstep; const char* b2 = last ? nB : cB + (size_t)(t + 2) * kstep;
;             const char* a3 = a2 + kstep; const char* b3 = b2 + kstep;
;             PG8_LDB(B0, 0, 0); PG8_LDB(B1, 0, 1); PG8_SCHED; PG8_LDA(At, 0, 0); PG8_STAGE_A(PG8_SA(1, 1), a1, 1, false);
;             PG8_WAIT_V(8); PG8_WAIT_L(0); PG8_BAR; PG8_MMA(0, 0, At, B0); PG8_MMA(0, 1, At, B1); PG8_BAR; PG8_SCHED;
;             PG8_LDA(At, 0, 1); PG8_STAGE(PG8_SB(0, 0), b2, voffB); PG8_STAGE(PG8_SB(0, 1), b2 + hstep, voffB); PG8_STAGE_A(PG8_SA(0, 0), a2, 0, last);
;             PG8_WAIT_V(8); PG8_WAIT_L(0); PG8_BAR; PG8_MMA(1, 0, At, B0); PG8_MMA(1, 1, At, B1); PG8_BAR; PG8_SCHED;
;             PG8_LDB(B0, 1, 0); PG8_LDB(B1, 1, 1); PG8_SCHED; PG8_LDA(At, 1, 0); PG8_STAGE_A(PG8_SA(0, 1), a2, 1, last);
;             PG8_WAIT_V(8); PG8_WAIT_L(0); PG8_BAR; PG8_MMA(0, 0, At, B0); PG8_MMA(0, 1, At, B1); PG8_BAR; PG8_SCHED;
;             PG8_LDA(At, 1, 1); PG8_STAGE(PG8_SB(1, 0), b3, voffB); PG8_STAGE(PG8_SB(1, 1), b3 + hstep, voffB); PG8_STAGE_A(PG8_SA(1, 0), a3, 0, last);
;             PG8_WAIT_V(8); PG8_WAIT_L(0); PG8_BAR; PG8_MMA(1, 0, At, B0); PG8_MMA(1, 1, At, B1); PG8_BAR; PG8_SCHED;
	s_setprio 1
	s_waitcnt lgkmcnt(0)
	v_mfma_f32_16x16x32_bf16 v[94:97], v[150:153], v[200:203], v[94:97]
	v_mfma_f32_16x16x32_bf16 v[90:93], v[176:179], v[200:203], v[90:93]
	v_mfma_f32_16x16x32_bf16 v[86:89], v[150:153], v[208:211], v[86:89]
	v_mfma_f32_16x16x32_bf16 v[82:85], v[176:179], v[208:211], v[82:85]
	v_mfma_f32_16x16x32_bf16 v[78:81], v[150:153], v[216:219], v[78:81]
	v_mfma_f32_16x16x32_bf16 v[74:77], v[176:179], v[216:219], v[74:77]
	v_mfma_f32_16x16x32_bf16 v[70:73], v[150:153], v[224:227], v[70:73]
	v_mfma_f32_16x16x32_bf16 v[66:69], v[176:179], v[224:227], v[66:69]
	v_mfma_f32_16x16x32_bf16 v[94:97], v[172:175], v[204:207], v[94:97]
	v_mfma_f32_16x16x32_bf16 v[90:93], v[180:183], v[204:207], v[90:93]
	v_mfma_f32_16x16x32_bf16 v[86:89], v[172:175], v[212:215], v[86:89]
	v_mfma_f32_16x16x32_bf16 v[82:85], v[180:183], v[212:215], v[82:85]
	v_mfma_f32_16x16x32_bf16 v[78:81], v[172:175], v[220:223], v[78:81]
	v_mfma_f32_16x16x32_bf16 v[74:77], v[180:183], v[220:223], v[74:77]
	v_mfma_f32_16x16x32_bf16 v[70:73], v[172:175], v[228:231], v[70:73]
	v_mfma_f32_16x16x32_bf16 v[66:69], v[180:183], v[228:231], v[66:69]
	s_setprio 0
	s_setprio 1
	v_mfma_f32_16x16x32_bf16 v[30:33], v[184:187], v[200:203], v[30:33]
	v_mfma_f32_16x16x32_bf16 v[26:29], v[192:195], v[200:203], v[26:29]
	v_mfma_f32_16x16x32_bf16 v[22:25], v[184:187], v[208:211], v[22:25]
	v_mfma_f32_16x16x32_bf16 v[18:21], v[192:195], v[208:211], v[18:21]
	v_mfma_f32_16x16x32_bf16 v[14:17], v[184:187], v[216:219], v[14:17]
	v_mfma_f32_16x16x32_bf16 v[10:13], v[192:195], v[216:219], v[10:13]
	v_mfma_f32_16x16x32_bf16 v[6:9], v[184:187], v[224:227], v[6:9]
	v_mfma_f32_16x16x32_bf16 v[2:5], v[192:195], v[224:227], v[2:5]
	v_mfma_f32_16x16x32_bf16 v[30:33], v[188:191], v[204:207], v[30:33]
	v_mfma_f32_16x16x32_bf16 v[26:29], v[196:199], v[204:207], v[26:29]
	v_mfma_f32_16x16x32_bf16 v[22:25], v[188:191], v[212:215], v[22:25]
	v_mfma_f32_16x16x32_bf16 v[18:21], v[196:199], v[212:215], v[18:21]
	v_mfma_f32_16x16x32_bf16 v[14:17], v[188:191], v[220:223], v[14:17]
	v_mfma_f32_16x16x32_bf16 v[10:13], v[196:199], v[220:223], v[10:13]
	v_mfma_f32_16x16x32_bf16 v[6:9], v[188:191], v[228:231], v[6:9]
	v_mfma_f32_16x16x32_bf16 v[2:5], v[196:199], v[228:231], v[2:5]
	s_setprio 0
	s_barrier
	s_add_i32 s56, 0, 0x18000
	v_add_u32_e32 v140, s56, v163
	s_add_i32 s57, 0, 0x1c000
	ds_read_b128 v[150:153], v140
	ds_read_b128 v[172:175], v140 offset:1024
	ds_read_b128 v[176:179], v140 offset:2048
	ds_read_b128 v[180:183], v140 offset:3072
	v_add_u32_e32 v140, s57, v163
	ds_read_b128 v[184:187], v140
	ds_read_b128 v[188:191], v140 offset:1024
	ds_read_b128 v[192:195], v140 offset:2048
	ds_read_b128 v[196:199], v140 offset:3072
	s_add_u32 s30, s30, 0x20000
	s_addc_u32 s31, s31, 0
	s_mov_b32 m0, s39
	v_lshl_add_u64 v[238:239], s[30:31], 0, v[132:133]
	ds_read_b128 v[200:203], v167 offset:32768
	ds_read_b128 v[204:207], v167 offset:33792
	ds_read_b128 v[208:211], v167 offset:34816
	ds_read_b128 v[212:215], v167 offset:35840
	ds_read_b128 v[216:219], v167 offset:36864
	ds_read_b128 v[220:223], v167 offset:37888
	ds_read_b128 v[224:227], v167 offset:38912
	ds_read_b128 v[228:231], v167 offset:39936
	global_load_lds_dwordx4 v[238:239], off
	v_lshl_add_u64 v[238:239], s[30:31], 0, v[136:137]
	s_mov_b32 m0, s40
	s_nop 0
	global_load_lds_dwordx4 v[238:239], off
	s_waitcnt vmcnt(8)
	s_waitcnt lgkmcnt(0)
	s_barrier
	s_setprio 1
	s_waitcnt lgkmcnt(0)
	v_mfma_f32_16x16x32_bf16 v[126:129], v[150:153], v[200:203], v[126:129]
	v_mfma_f32_16x16x32_bf16 v[122:125], v[176:179], v[200:203], v[122:125]
	v_mfma_f32_16x16x32_bf16 v[118:121], v[150:153], v[208:211], v[118:121]
	v_mfma_f32_16x16x32_bf16 v[114:117], v[176:179], v[208:211], v[114:117]
	v_mfma_f32_16x16x32_bf16 v[110:113], v[150:153], v[216:219], v[110:113]
	v_mfma_f32_16x16x32_bf16 v[106:109], v[176:179], v[216:219], v[106:109]
	v_mfma_f32_16x16x32_bf16 v[102:105], v[150:153], v[224:227], v[102:105]
	v_mfma_f32_16x16x32_bf16 v[98:101], v[176:179], v[224:227], v[98:101]
	v_mfma_f32_16x16x32_bf16 v[126:129], v[172:175], v[204:207], v[126:129]
	v_mfma_f32_16x16x32_bf16 v[122:125], v[180:183], v[204:207], v[122:125]
	v_mfma_f32_16x16x32_bf16 v[118:121], v[172:175], v[212:215], v[118:121]
	v_mfma_f32_16x16x32_bf16 v[114:117], v[180:183], v[212:215], v[114:117]
	v_mfma_f32_16x16x32_bf16 v[110:113], v[172:175], v[220:223], v[110:113]
	v_mfma_f32_16x16x32_bf16 v[106:109], v[180:183], v[220:223], v[106:109]
	v_mfma_f32_16x16x32_bf16 v[102:105], v[172:175], v[228:231], v[102:105]
	v_mfma_f32_16x16x32_bf16 v[98:101], v[180:183], v[228:231], v[98:101]
	s_setprio 0
	s_setprio 1
	v_mfma_f32_16x16x32_bf16 v[62:65], v[184:187], v[200:203], v[62:65]
	v_mfma_f32_16x16x32_bf16 v[58:61], v[192:195], v[200:203], v[58:61]
	v_mfma_f32_16x16x32_bf16 v[54:57], v[184:187], v[208:211], v[54:57]
	v_mfma_f32_16x16x32_bf16 v[50:53], v[192:195], v[208:211], v[50:53]
	v_mfma_f32_16x16x32_bf16 v[46:49], v[184:187], v[216:219], v[46:49]
	v_mfma_f32_16x16x32_bf16 v[42:45], v[192:195], v[216:219], v[42:45]
	v_mfma_f32_16x16x32_bf16 v[38:41], v[184:187], v[224:227], v[38:41]
	v_mfma_f32_16x16x32_bf16 v[34:37], v[192:195], v[224:227], v[34:37]
	v_mfma_f32_16x16x32_bf16 v[62:65], v[188:191], v[204:207], v[62:65]
	v_mfma_f32_16x16x32_bf16 v[58:61], v[196:199], v[204:207], v[58:61]
	v_mfma_f32_16x16x32_bf16 v[54:57], v[188:191], v[212:215], v[54:57]
	v_mfma_f32_16x16x32_bf16 v[50:53], v[196:199], v[212:215], v[50:53]
	v_mfma_f32_16x16x32_bf16 v[46:49], v[188:191], v[220:223], v[46:49]
	v_mfma_f32_16x16x32_bf16 v[42:45], v[196:199], v[220:223], v[42:45]
	v_mfma_f32_16x16x32_bf16 v[38:41], v[188:191], v[228:231], v[38:41]
	v_mfma_f32_16x16x32_bf16 v[34:37], v[196:199], v[228:231], v[34:37]
	s_setprio 0
	s_barrier
; #define PG8_STAGE(bufoff, gbase, voff) do { _Pragma("unroll") for (int _i = 0; _i < 2; ++_i) \
;         __builtin_amdgcn_global_load_lds((const unsigned*)((const char*)(gbase) + (voff)[_i]), (LAS unsigned*)(lds + (bufoff) + ldsw + _i * 8192), 16, 0, 0); } while (0)
; #define PG8_LDA(dst, b, h) do { if constexpr (FP8) { _Pragma("unroll") for (int m = 0; m < 4; ++m) dst##8[m] = PG8_LD8(lds + PG8_SA(b, h) + aoff + m * 2048); } \
;         else { _Pragma("unroll") for (int m = 0; m < 4; ++m) _Pragma("unroll") for (int k = 0; k < 2; ++k) dst[m][k] = *(const LAS bf16x8*)(lds + PG8_SA(b, h) + aoff + m * 2048 + k * 1024); } } while (0)
; #define PG8_WAIT_V(n) asm volatile("s_waitcnt vmcnt(" #n ")" ::: "memory")
; #define PG8_WAIT_L(n) asm volatile("s_waitcnt lgkmcnt(" #n ")" ::: "memory")
; template <class Epi, class Sched, bool GATHER, bool FP8 = false>
; __device__ __forceinline__ void gemm_phase(LAS unsigned char* lds, const Gemm g, const Sched& S, const Epi& E) {
;     ...
;         for (int t = 0; t < nt; t += 2) {
;             const bool last = (t == nt - 2);
;             const char* a1 = cA + (size_t)(t + 1) * kstep;
;             const char* a2 = last ? nA : cA + (size_t)(t + 2) * kstep; const char* b2 = last ? nB : cB + (size_t)(t + 2) * kstep;
;             const char* a3 = a2 + kstep; const char* b3 = b2 + kstep;
;             PG8_LDB(B0, 0, 0); PG8_LDB(B1, 0, 1); PG8_SCHED; PG8_LDA(At, 0, 0); PG8_STAGE_A(PG8_SA(1, 1), a1, 1, false);
;             PG8_WAIT_V(8); PG8_WAIT_L(0); PG8_BAR; PG8_MMA(0, 0, At, B0); PG8_MMA(0, 1, At, B1); PG8_BAR; PG8_SCHED;
;             PG8_LDA(At, 0, 1); PG8_STAGE(PG8_SB(0, 0), b2, voffB); PG8_STAGE(PG8_SB(0, 1), b2 + hstep, voffB); PG8_STAGE_A(PG8_SA(0, 0), a2, 0, last);
;             PG8_WAIT_V(8); PG8_WAIT_L(0); PG8_BAR; PG8_MMA(1, 0, At, B0); PG8_MMA(1, 1, At, B1); PG8_BAR; PG8_SCHED;
;             PG8_LDB(B0, 1, 0); PG8_LDB(B1, 1, 1); PG8_SCHED; PG8_LDA(At, 1, 0); PG8_STAGE_A(PG8_SA(0, 1), a2, 1, last);
;             PG8_WAIT_V(8); PG8_WAIT_L(0); PG8_BAR; PG8_MMA(0, 0, At, B0); PG8_MMA(0, 1, At, B1); PG8_BAR; PG8_SCHED;
;             PG8_LDA(At, 1, 1); PG8_STAGE(PG8_SB(1, 0), b3, voffB); PG8_STAGE(PG8_SB(1, 1), b3 + hstep, voffB); PG8_STAGE_A(PG8_SA(1, 0), a3, 0, last);
;             PG8_WAIT_V(8); PG8_WAIT_L(0); PG8_BAR; PG8_MMA(1, 0, At, B0); PG8_MMA(1, 1, At, B1); PG8_BAR; PG8_SCHED;
	s_add_i32 s30, s56, s37
	v_lshl_add_u64 v[168:169], v[168:169], 0, s[8:9]
	s_mov_b32 m0, s30
	ds_read_b128 v[200:203], v167 offset:49152
	ds_read_b128 v[204:207], v167 offset:50176
	ds_read_b128 v[208:211], v167 offset:51200
	ds_read_b128 v[212:215], v167 offset:52224
	ds_read_b128 v[216:219], v167 offset:53248
	ds_read_b128 v[220:223], v167 offset:54272
	ds_read_b128 v[224:227], v167 offset:55296
	ds_read_b128 v[228:231], v167 offset:56320
	global_load_lds_dwordx4 v[168:169], off
	s_add_i32 m0, s30, 0x2000
	s_add_u32 s28, s28, 0x20080
	v_lshl_add_u64 v[168:169], v[232:233], 0, s[8:9]
	s_addc_u32 s29, s29, 0
	s_add_i32 s30, s57, s37
	global_load_lds_dwordx4 v[168:169], off
	v_lshl_add_u64 v[168:169], s[28:29], 0, v[134:135]
	s_mov_b32 m0, s30
	s_nop 0
	global_load_lds_dwordx4 v[168:169], off
	v_lshl_add_u64 v[168:169], s[28:29], 0, v[138:139]
	s_add_i32 m0, s30, 0x2000
	s_nop 0
	global_load_lds_dwordx4 v[168:169], off
	v_lshl_add_u64 v[168:169], v[234:235], 0, s[8:9]
	s_mov_b32 m0, s42
	s_nop 0
	global_load_lds_dwordx4 v[168:169], off
	v_lshl_add_u64 v[168:169], v[236:237], 0, s[8:9]
	s_mov_b32 m0, s43
	s_nop 0
	global_load_lds_dwordx4 v[168:169], off
	s_waitcnt vmcnt(8)
	s_waitcnt lgkmcnt(0)
	s_barrier
	s_setprio 1
	s_waitcnt lgkmcnt(0)
	v_mfma_f32_16x16x32_bf16 v[94:97], v[150:153], v[200:203], v[94:97]
	v_mfma_f32_16x16x32_bf16 v[90:93], v[176:179], v[200:203], v[90:93]
	v_mfma_f32_16x16x32_bf16 v[86:89], v[150:153], v[208:211], v[86:89]
	v_mfma_f32_16x16x32_bf16 v[82:85], v[176:179], v[208:211], v[82:85]
	v_mfma_f32_16x16x32_bf16 v[78:81], v[150:153], v[216:219], v[78:81]
	v_mfma_f32_16x16x32_bf16 v[74:77], v[176:179], v[216:219], v[74:77]
	v_mfma_f32_16x16x32_bf16 v[70:73], v[150:153], v[224:227], v[70:73]
	v_mfma_f32_16x16x32_bf16 v[66:69], v[176:179], v[224:227], v[66:69]
	v_mfma_f32_16x16x32_bf16 v[94:97], v[172:175], v[204:207], v[94:97]
	v_mfma_f32_16x16x32_bf16 v[90:93], v[180:183], v[204:207], v[90:93]
	v_mfma_f32_16x16x32_bf16 v[86:89], v[172:175], v[212:215], v[86:89]
	v_mfma_f32_16x16x32_bf16 v[82:85], v[180:183], v[212:215], v[82:85]
	v_mfma_f32_16x16x32_bf16 v[78:81], v[172:175], v[220:223], v[78:81]
	v_mfma_f32_16x16x32_bf16 v[74:77], v[180:183], v[220:223], v[74:77]
	v_mfma_f32_16x16x32_bf16 v[70:73], v[172:175], v[228:231], v[70:73]
	v_mfma_f32_16x16x32_bf16 v[66:69], v[180:183], v[228:231], v[66:69]
	s_setprio 0
	s_setprio 1
	v_mfma_f32_16x16x32_bf16 v[30:33], v[184:187], v[200:203], v[30:33]
	v_mfma_f32_16x16x32_bf16 v[26:29], v[192:195], v[200:203], v[26:29]
	v_mfma_f32_16x16x32_bf16 v[22:25], v[184:187], v[208:211], v[22:25]
	v_mfma_f32_16x16x32_bf16 v[18:21], v[192:195], v[208:211], v[18:21]
	v_mfma_f32_16x16x32_bf16 v[14:17], v[184:187], v[216:219], v[14:17]
	v_mfma_f32_16x16x32_bf16 v[10:13], v[192:195], v[216:219], v[10:13]
	v_mfma_f32_16x16x32_bf16 v[6:9], v[184:187], v[224:227], v[6:9]
	v_mfma_f32_16x16x32_bf16 v[2:5], v[192:195], v[224:227], v[2:5]
	v_mfma_f32_16x16x32_bf16 v[30:33], v[188:191], v[204:207], v[30:33]
	v_mfma_f32_16x16x32_bf16 v[26:29], v[196:199], v[204:207], v[26:29]
	v_mfma_f32_16x16x32_bf16 v[22:25], v[188:191], v[212:215], v[22:25]
	v_mfma_f32_16x16x32_bf16 v[18:21], v[196:199], v[212:215], v[18:21]
	v_mfma_f32_16x16x32_bf16 v[14:17], v[188:191], v[220:223], v[14:17]
	v_mfma_f32_16x16x32_bf16 v[10:13], v[196:199], v[220:223], v[10:13]
	v_mfma_f32_16x16x32_bf16 v[6:9], v[188:191], v[228:231], v[6:9]
	v_mfma_f32_16x16x32_bf16 v[2:5], v[196:199], v[228:231], v[2:5]
	s_setprio 0
	s_add_i32 s55, s55, 2
	s_add_u32 s26, s26, 0x100
	s_addc_u32 s27, s27, 0
	s_add_u32 s53, s53, 0x100
	s_addc_u32 s54, s54, 0
	s_cmp_gt_u32 s55, 5
	s_barrier
	s_cbranch_scc0 .LBB0_279
	s_and_b64 vcc, exec, s[10:11]
	s_cbranch_vccz .LBB0_282
	s_barrier

; #define PG8_STAGE(bufoff, gbase, voff) do { _Pragma("unroll") for (int _i = 0; _i < 2; ++_i) \
;         __builtin_amdgcn_global_load_lds((const unsigned*)((const char*)(gbase) + (voff)[_i]), (LAS unsigned*)(lds + (bufoff) + ldsw + _i * 8192), 16, 0, 0); } while (0)
; #define PG8_LDA(dst, b, h) do { if constexpr (FP8) { _Pragma("unroll") for (int m = 0; m < 4; ++m) dst##8[m] = PG8_LD8(lds + PG8_SA(b, h) + aoff + m * 2048); } \
;         else { _Pragma("unroll") for (int m = 0; m < 4; ++m) _Pragma("unroll") for (int k = 0; k < 2; ++k) dst[m][k] = *(const LAS bf16x8*)(lds + PG8_SA(b, h) + aoff + m * 2048 + k * 1024); } } while (0)
; #define PG8_WAIT_V(n) asm volatile("s_waitcnt vmcnt(" #n ")" ::: "memory")
; #define PG8_WAIT_L(n) asm volatile("s_waitcnt lgkmcnt(" #n ")" ::: "memory")
; template <class Epi, class Sched, bool GATHER, bool FP8 = false>
; __device__ __forceinline__ void gemm_phase(LAS unsigned char* lds, const Gemm g, const Sched& S, const Epi& E) {
;     ...
;         for (int t = 0; t < nt; t += 2) {
;             const bool last = (t == nt - 2);
;             const char* a1 = cA + (size_t)(t + 1) * kstep;
;             const char* a2 = last ? nA : cA + (size_t)(t + 2) * kstep; const char* b2 = last ? nB : cB + (size_t)(t + 2) * kstep;
;             const char* a3 = a2 + kstep; const char* b3 = b2 + kstep;
;             PG8_LDB(B0, 0, 0); PG8_LDB(B1, 0, 1); PG8_SCHED; PG8_LDA(At, 0, 0); PG8_STAGE_A(PG8_SA(1, 1), a1, 1, false);
;             PG8_WAIT_V(8); PG8_WAIT_L(0); PG8_BAR; PG8_MMA(0, 0, At, B0); PG8_MMA(0, 1, At, B1); PG8_BAR; PG8_SCHED;
;             PG8_LDA(At, 0, 1); PG8_STAGE(PG8_SB(0, 0), b2, voffB); PG8_STAGE(PG8_SB(0, 1), b2 + hstep, voffB); PG8_STAGE_A(PG8_SA(0, 0), a2, 0, last);
;             PG8_WAIT_V(8); PG8_WAIT_L(0); PG8_BAR; PG8_MMA(1, 0, At, B0); PG8_MMA(1, 1, At, B1); PG8_BAR; PG8_SCHED;
;             PG8_LDB(B0, 1, 0); PG8_LDB(B1, 1, 1); PG8_SCHED; PG8_LDA(At, 1, 0); PG8_STAGE_A(PG8_SA(0, 1), a2, 1, last);
;             PG8_WAIT_V(8); PG8_WAIT_L(0); PG8_BAR; PG8_MMA(0, 0, At, B0); PG8_MMA(0, 1, At, B1); PG8_BAR; PG8_SCHED;
;             PG8_LDA(At, 1, 1); PG8_STAGE(PG8_SB(1, 0), b3, voffB); PG8_STAGE(PG8_SB(1, 1), b3 + hstep, voffB); PG8_STAGE_A(PG8_SA(1, 0), a3, 0, last);
;             PG8_WAIT_V(8); PG8_WAIT_L(0); PG8_BAR; PG8_MMA(1, 0, At, B0); PG8_MMA(1, 1, At, B1); PG8_BAR; PG8_SCHED;
.LBB0_335:
	ds_read_b128 v[156:159], v1
	ds_read_b128 v[160:163], v1 offset:1024
	ds_read_b128 v[164:167], v1 offset:2048
	ds_read_b128 v[172:175], v1 offset:3072
	ds_read_b128 v[176:179], v153
	ds_read_b128 v[180:183], v153 offset:1024
	ds_read_b128 v[184:187], v153 offset:2048
	ds_read_b128 v[188:191], v153 offset:3072
	s_add_u32 s30, s28, 0xfffe0080
	s_addc_u32 s31, s29, -1
	s_cmp_eq_u32 s59, 4
	s_cselect_b32 s35, s21, s31
	s_cselect_b32 s34, s55, s30
	s_cselect_b32 s31, s19, s58
	s_cselect_b32 s30, s56, s57
	v_lshl_add_u64 v[148:149], s[28:29], 0, v[140:141]
	s_add_i32 m0, s27, 0xc000
	ds_read_b128 v[192:195], v155
	ds_read_b128 v[196:199], v155 offset:1024
	ds_read_b128 v[200:203], v155 offset:2048
	ds_read_b128 v[204:207], v155 offset:3072
	ds_read_b128 v[208:211], v155 offset:4096
	ds_read_b128 v[212:215], v155 offset:5120
	ds_read_b128 v[216:219], v155 offset:6144
	ds_read_b128 v[220:223], v155 offset:7168
	global_load_lds_dwordx4 v[148:149], off
	v_lshl_add_u64 v[148:149], s[28:29], 0, v[142:143]
	s_add_i32 m0, s27, 0xe000
	s_nop 0
	global_load_lds_dwordx4 v[148:149], off
	s_waitcnt vmcnt(8)
	s_waitcnt lgkmcnt(0)
	s_barrier
	s_setprio 1
	s_waitcnt lgkmcnt(0)
	v_mfma_f32_16x16x32_bf16 v[126:129], v[156:159], v[192:195], v[126:129]
	v_mfma_f32_16x16x32_bf16 v[122:125], v[164:167], v[192:195], v[122:125]
	v_mfma_f32_16x16x32_bf16 v[118:121], v[156:159], v[200:203], v[118:121]
	v_mfma_f32_16x16x32_bf16 v[110:113], v[164:167], v[200:203], v[110:113]
	v_mfma_f32_16x16x32_bf16 v[102:105], v[156:159], v[208:211], v[102:105]
	v_mfma_f32_16x16x32_bf16 v[94:97], v[164:167], v[208:211], v[94:97]
	v_mfma_f32_16x16x32_bf16 v[86:89], v[156:159], v[216:219], v[86:89]
	v_mfma_f32_16x16x32_bf16 v[78:81], v[164:167], v[216:219], v[78:81]
	v_mfma_f32_16x16x32_bf16 v[126:129], v[160:163], v[196:199], v[126:129]
	v_mfma_f32_16x16x32_bf16 v[122:125], v[172:175], v[196:199], v[122:125]
	v_mfma_f32_16x16x32_bf16 v[118:121], v[160:163], v[204:207], v[118:121]
	v_mfma_f32_16x16x32_bf16 v[110:113], v[172:175], v[204:207], v[110:113]
	v_mfma_f32_16x16x32_bf16 v[102:105], v[160:163], v[212:215], v[102:105]
	v_mfma_f32_16x16x32_bf16 v[94:97], v[172:175], v[212:215], v[94:97]
	v_mfma_f32_16x16x32_bf16 v[86:89], v[160:163], v[220:223], v[86:89]
	v_mfma_f32_16x16x32_bf16 v[78:81], v[172:175], v[220:223], v[78:81]
	s_setprio 0
	s_setprio 1
	v_mfma_f32_16x16x32_bf16 v[114:117], v[176:179], v[192:195], v[114:117]
	v_mfma_f32_16x16x32_bf16 v[106:109], v[184:187], v[192:195], v[106:109]
	v_mfma_f32_16x16x32_bf16 v[98:101], v[176:179], v[200:203], v[98:101]
	v_mfma_f32_16x16x32_bf16 v[90:93], v[184:187], v[200:203], v[90:93]
	v_mfma_f32_16x16x32_bf16 v[82:85], v[176:179], v[208:211], v[82:85]
	v_mfma_f32_16x16x32_bf16 v[74:77], v[184:187], v[208:211], v[74:77]
	v_mfma_f32_16x16x32_bf16 v[70:73], v[176:179], v[216:219], v[70:73]
	v_mfma_f32_16x16x32_bf16 v[66:69], v[184:187], v[216:219], v[66:69]
	v_mfma_f32_16x16x32_bf16 v[114:117], v[180:183], v[196:199], v[114:117]
	v_mfma_f32_16x16x32_bf16 v[106:109], v[188:191], v[196:199], v[106:109]
	v_mfma_f32_16x16x32_bf16 v[98:101], v[180:183], v[204:207], v[98:101]
	v_mfma_f32_16x16x32_bf16 v[90:93], v[188:191], v[204:207], v[90:93]
	v_mfma_f32_16x16x32_bf16 v[82:85], v[180:183], v[212:215], v[82:85]
	v_mfma_f32_16x16x32_bf16 v[74:77], v[188:191], v[212:215], v[74:77]
	v_mfma_f32_16x16x32_bf16 v[70:73], v[180:183], v[220:223], v[70:73]
	v_mfma_f32_16x16x32_bf16 v[66:69], v[188:191], v[220:223], v[66:69]
	s_setprio 0
	s_barrier
	s_add_i32 s60, s48, s40
	v_lshl_add_u64 v[148:149], s[30:31], 0, v[134:135]
	s_mov_b32 m0, s60
	ds_read_b128 v[192:195], v155 offset:16384
	ds_read_b128 v[196:199], v155 offset:17408
	ds_read_b128 v[200:203], v155 offset:18432
	ds_read_b128 v[204:207], v155 offset:19456
	ds_read_b128 v[208:211], v155 offset:20480
	ds_read_b128 v[212:215], v155 offset:21504
	ds_read_b128 v[216:219], v155 offset:22528
	ds_read_b128 v[220:223], v155 offset:23552
	global_load_lds_dwordx4 v[148:149], off
	s_add_i32 m0, s60, 0x2000
	s_add_u32 s60, s30, 0x20000
	v_lshl_add_u64 v[168:169], s[30:31], 0, v[138:139]
	s_addc_u32 s61, s31, 0
	s_add_i32 s62, s49, s40
	global_load_lds_dwordx4 v[168:169], off
	v_lshl_add_u64 v[224:225], s[60:61], 0, v[134:135]
	s_mov_b32 m0, s62
	v_lshl_add_u64 v[226:227], s[34:35], 0, v[136:137]
	global_load_lds_dwordx4 v[224:225], off
	v_lshl_add_u64 v[224:225], s[60:61], 0, v[138:139]
	s_add_i32 m0, s62, 0x2000
	s_nop 0
	global_load_lds_dwordx4 v[224:225], off
	v_lshl_add_u64 v[224:225], s[34:35], 0, v[132:133]
	s_mov_b32 m0, s27
	s_nop 0
	global_load_lds_dwordx4 v[224:225], off
	s_mov_b32 m0, s41
	s_nop 0
	global_load_lds_dwordx4 v[226:227], off
	s_waitcnt vmcnt(8)
	s_waitcnt lgkmcnt(0)
	s_barrier
; #define PG8_STAGE(bufoff, gbase, voff) do { _Pragma("unroll") for (int _i = 0; _i < 2; ++_i) \
;         __builtin_amdgcn_global_load_lds((const unsigned*)((const char*)(gbase) + (voff)[_i]), (LAS unsigned*)(lds + (bufoff) + ldsw + _i * 8192), 16, 0, 0); } while (0)
; #define PG8_LDA(dst, b, h) do { if constexpr (FP8) { _Pragma("unroll") for (int m = 0; m < 4; ++m) dst##8[m] = PG8_LD8(lds + PG8_SA(b, h) + aoff + m * 2048); } \
;         else { _Pragma("unroll") for (int m = 0; m < 4; ++m) _Pragma("unroll") for (int k = 0; k < 2; ++k) dst[m][k] = *(const LAS bf16x8*)(lds + PG8_SA(b, h) + aoff + m * 2048 + k * 1024); } } while (0)
; #define PG8_WAIT_V(n) asm volatile("s_waitcnt vmcnt(" #n ")" ::: "memory")
; #define PG8_WAIT_L(n) asm volatile("s_waitcnt lgkmcnt(" #n ")" ::: "memory")
; template <class Epi, class Sched, bool GATHER, bool FP8 = false>
; __device__ __forceinline__ void gemm_phase(LAS unsigned char* lds, const Gemm g, const Sched& S, const Epi& E) {
;     ...
;         for (int t = 0; t < nt; t += 2) {
;             const bool last = (t == nt - 2);
;             const char* a1 = cA + (size_t)(t + 1) * kstep;
;             const char* a2 = last ? nA : cA + (size_t)(t + 2) * kstep; const char* b2 = last ? nB : cB + (size_t)(t + 2) * kstep;
;             const char* a3 = a2 + kstep; const char* b3 = b2 + kstep;
;             PG8_LDB(B0, 0, 0); PG8_LDB(B1, 0, 1); PG8_SCHED; PG8_LDA(At, 0, 0); PG8_STAGE_A(PG8_SA(1, 1), a1, 1, false);
;             PG8_WAIT_V(8); PG8_WAIT_L(0); PG8_BAR; PG8_MMA(0, 0, At, B0); PG8_MMA(0, 1, At, B1); PG8_BAR; PG8_SCHED;
;             PG8_LDA(At, 0, 1); PG8_STAGE(PG8_SB(0, 0), b2, voffB); PG8_STAGE(PG8_SB(0, 1), b2 + hstep, voffB); PG8_STAGE_A(PG8_SA(0, 0), a2, 0, last);
;             PG8_WAIT_V(8); PG8_WAIT_L(0); PG8_BAR; PG8_MMA(1, 0, At, B0); PG8_MMA(1, 1, At, B1); PG8_BAR; PG8_SCHED;
;             PG8_LDB(B0, 1, 0); PG8_LDB(B1, 1, 1); PG8_SCHED; PG8_LDA(At, 1, 0); PG8_STAGE_A(PG8_SA(0, 1), a2, 1, last);
;             PG8_WAIT_V(8); PG8_WAIT_L(0); PG8_BAR; PG8_MMA(0, 0, At, B0); PG8_MMA(0, 1, At, B1); PG8_BAR; PG8_SCHED;
;             PG8_LDA(At, 1, 1); PG8_STAGE(PG8_SB(1, 0), b3, voffB); PG8_STAGE(PG8_SB(1, 1), b3 + hstep, voffB); PG8_STAGE_A(PG8_SA(1, 0), a3, 0, last);
;             PG8_WAIT_V(8); PG8_WAIT_L(0); PG8_BAR; PG8_MMA(1, 0, At, B0); PG8_MMA(1, 1, At, B1); PG8_BAR; PG8_SCHED;
	s_setprio 1
	s_waitcnt lgkmcnt(0)
	v_mfma_f32_16x16x32_bf16 v[62:65], v[156:159], v[192:195], v[62:65]
	v_mfma_f32_16x16x32_bf16 v[58:61], v[164:167], v[192:195], v[58:61]
	v_mfma_f32_16x16x32_bf16 v[54:57], v[156:159], v[200:203], v[54:57]
	v_mfma_f32_16x16x32_bf16 v[46:49], v[164:167], v[200:203], v[46:49]
	v_mfma_f32_16x16x32_bf16 v[38:41], v[156:159], v[208:211], v[38:41]
	v_mfma_f32_16x16x32_bf16 v[30:33], v[164:167], v[208:211], v[30:33]
	v_mfma_f32_16x16x32_bf16 v[22:25], v[156:159], v[216:219], v[22:25]
	v_mfma_f32_16x16x32_bf16 v[14:17], v[164:167], v[216:219], v[14:17]
	v_mfma_f32_16x16x32_bf16 v[62:65], v[160:163], v[196:199], v[62:65]
	v_mfma_f32_16x16x32_bf16 v[58:61], v[172:175], v[196:199], v[58:61]
	v_mfma_f32_16x16x32_bf16 v[54:57], v[160:163], v[204:207], v[54:57]
	v_mfma_f32_16x16x32_bf16 v[46:49], v[172:175], v[204:207], v[46:49]
	v_mfma_f32_16x16x32_bf16 v[38:41], v[160:163], v[212:215], v[38:41]
	v_mfma_f32_16x16x32_bf16 v[30:33], v[172:175], v[212:215], v[30:33]
	v_mfma_f32_16x16x32_bf16 v[22:25], v[160:163], v[220:223], v[22:25]
	v_mfma_f32_16x16x32_bf16 v[14:17], v[172:175], v[220:223], v[14:17]
	s_setprio 0
	s_setprio 1
	v_mfma_f32_16x16x32_bf16 v[50:53], v[176:179], v[192:195], v[50:53]
	v_mfma_f32_16x16x32_bf16 v[42:45], v[184:187], v[192:195], v[42:45]
	v_mfma_f32_16x16x32_bf16 v[34:37], v[176:179], v[200:203], v[34:37]
	v_mfma_f32_16x16x32_bf16 v[26:29], v[184:187], v[200:203], v[26:29]
	v_mfma_f32_16x16x32_bf16 v[18:21], v[176:179], v[208:211], v[18:21]
	v_mfma_f32_16x16x32_bf16 v[10:13], v[184:187], v[208:211], v[10:13]
	v_mfma_f32_16x16x32_bf16 v[6:9], v[176:179], v[216:219], v[6:9]
	v_mfma_f32_16x16x32_bf16 v[2:5], v[184:187], v[216:219], v[2:5]
	v_mfma_f32_16x16x32_bf16 v[50:53], v[180:183], v[196:199], v[50:53]
	v_mfma_f32_16x16x32_bf16 v[42:45], v[188:191], v[196:199], v[42:45]
	v_mfma_f32_16x16x32_bf16 v[34:37], v[180:183], v[204:207], v[34:37]
	v_mfma_f32_16x16x32_bf16 v[26:29], v[188:191], v[204:207], v[26:29]
	v_mfma_f32_16x16x32_bf16 v[18:21], v[180:183], v[212:215], v[18:21]
	v_mfma_f32_16x16x32_bf16 v[10:13], v[188:191], v[212:215], v[10:13]
	v_mfma_f32_16x16x32_bf16 v[6:9], v[180:183], v[220:223], v[6:9]
	v_mfma_f32_16x16x32_bf16 v[2:5], v[188:191], v[220:223], v[2:5]
	s_setprio 0
	s_barrier
	s_add_i32 s60, 0, 0x18000
	v_add_u32_e32 v171, s60, v151
	s_add_i32 s61, 0, 0x1c000
	ds_read_b128 v[156:159], v171
	ds_read_b128 v[160:163], v171 offset:1024
	ds_read_b128 v[164:167], v171 offset:2048
	ds_read_b128 v[172:175], v171 offset:3072
	v_add_u32_e32 v171, s61, v151
	ds_read_b128 v[176:179], v171
	ds_read_b128 v[180:183], v171 offset:1024
	ds_read_b128 v[184:187], v171 offset:2048
	ds_read_b128 v[188:191], v171 offset:3072
	s_add_u32 s34, s34, 0x20000
	s_addc_u32 s35, s35, 0
	s_mov_b32 m0, s42
	v_lshl_add_u64 v[228:229], s[34:35], 0, v[132:133]
	ds_read_b128 v[192:195], v155 offset:32768
	ds_read_b128 v[196:199], v155 offset:33792
	ds_read_b128 v[200:203], v155 offset:34816
	ds_read_b128 v[204:207], v155 offset:35840
	ds_read_b128 v[208:211], v155 offset:36864
	ds_read_b128 v[212:215], v155 offset:37888
	ds_read_b128 v[216:219], v155 offset:38912
	ds_read_b128 v[220:223], v155 offset:39936
	global_load_lds_dwordx4 v[228:229], off
	v_lshl_add_u64 v[228:229], s[34:35], 0, v[136:137]
	s_mov_b32 m0, s43
	s_nop 0
	global_load_lds_dwordx4 v[228:229], off
	s_waitcnt vmcnt(8)
	s_waitcnt lgkmcnt(0)
	s_barrier
	s_setprio 1
	s_waitcnt lgkmcnt(0)
	v_mfma_f32_16x16x32_bf16 v[126:129], v[156:159], v[192:195], v[126:129]
	v_mfma_f32_16x16x32_bf16 v[122:125], v[164:167], v[192:195], v[122:125]
	v_mfma_f32_16x16x32_bf16 v[118:121], v[156:159], v[200:203], v[118:121]
	v_mfma_f32_16x16x32_bf16 v[110:113], v[164:167], v[200:203], v[110:113]
	v_mfma_f32_16x16x32_bf16 v[102:105], v[156:159], v[208:211], v[102:105]
	v_mfma_f32_16x16x32_bf16 v[94:97], v[164:167], v[208:211], v[94:97]
	v_mfma_f32_16x16x32_bf16 v[86:89], v[156:159], v[216:219], v[86:89]
	v_mfma_f32_16x16x32_bf16 v[78:81], v[164:167], v[216:219], v[78:81]
	v_mfma_f32_16x16x32_bf16 v[126:129], v[160:163], v[196:199], v[126:129]
	v_mfma_f32_16x16x32_bf16 v[122:125], v[172:175], v[196:199], v[122:125]
	v_mfma_f32_16x16x32_bf16 v[118:121], v[160:163], v[204:207], v[118:121]
	v_mfma_f32_16x16x32_bf16 v[110:113], v[172:175], v[204:207], v[110:113]
	v_mfma_f32_16x16x32_bf16 v[102:105], v[160:163], v[212:215], v[102:105]
	v_mfma_f32_16x16x32_bf16 v[94:97], v[172:175], v[212:215], v[94:97]
	v_mfma_f32_16x16x32_bf16 v[86:89], v[160:163], v[220:223], v[86:89]
	v_mfma_f32_16x16x32_bf16 v[78:81], v[172:175], v[220:223], v[78:81]
	s_setprio 0
	s_setprio 1
	v_mfma_f32_16x16x32_bf16 v[114:117], v[176:179], v[192:195], v[114:117]
	v_mfma_f32_16x16x32_bf16 v[106:109], v[184:187], v[192:195], v[106:109]
	v_mfma_f32_16x16x32_bf16 v[98:101], v[176:179], v[200:203], v[98:101]
	v_mfma_f32_16x16x32_bf16 v[90:93], v[184:187], v[200:203], v[90:93]
	v_mfma_f32_16x16x32_bf16 v[82:85], v[176:179], v[208:211], v[82:85]
	v_mfma_f32_16x16x32_bf16 v[74:77], v[184:187], v[208:211], v[74:77]
	v_mfma_f32_16x16x32_bf16 v[70:73], v[176:179], v[216:219], v[70:73]
	v_mfma_f32_16x16x32_bf16 v[66:69], v[184:187], v[216:219], v[66:69]
	v_mfma_f32_16x16x32_bf16 v[114:117], v[180:183], v[196:199], v[114:117]
	v_mfma_f32_16x16x32_bf16 v[106:109], v[188:191], v[196:199], v[106:109]
	v_mfma_f32_16x16x32_bf16 v[98:101], v[180:183], v[204:207], v[98:101]
	v_mfma_f32_16x16x32_bf16 v[90:93], v[188:191], v[204:207], v[90:93]
	v_mfma_f32_16x16x32_bf16 v[82:85], v[180:183], v[212:215], v[82:85]
	v_mfma_f32_16x16x32_bf16 v[74:77], v[188:191], v[212:215], v[74:77]
	v_mfma_f32_16x16x32_bf16 v[70:73], v[180:183], v[220:223], v[70:73]
	v_mfma_f32_16x16x32_bf16 v[66:69], v[188:191], v[220:223], v[66:69]
	s_setprio 0
	s_barrier
; #define PG8_STAGE(bufoff, gbase, voff) do { _Pragma("unroll") for (int _i = 0; _i < 2; ++_i) \
;         __builtin_amdgcn_global_load_lds((const unsigned*)((const char*)(gbase) + (voff)[_i]), (LAS unsigned*)(lds + (bufoff) + ldsw + _i * 8192), 16, 0, 0); } while (0)
; #define PG8_LDA(dst, b, h) do { if constexpr (FP8) { _Pragma("unroll") for (int m = 0; m < 4; ++m) dst##8[m] = PG8_LD8(lds + PG8_SA(b, h) + aoff + m * 2048); } \
;         else { _Pragma("unroll") for (int m = 0; m < 4; ++m) _Pragma("unroll") for (int k = 0; k < 2; ++k) dst[m][k] = *(const LAS bf16x8*)(lds + PG8_SA(b, h) + aoff + m * 2048 + k * 1024); } } while (0)
; #define PG8_WAIT_V(n) asm volatile("s_waitcnt vmcnt(" #n ")" ::: "memory")
; #define PG8_WAIT_L(n) asm volatile("s_waitcnt lgkmcnt(" #n ")" ::: "memory")
; template <class Epi, class Sched, bool GATHER, bool FP8 = false>
; __device__ __forceinline__ void gemm_phase(LAS unsigned char* lds, const Gemm g, const Sched& S, const Epi& E) {
;     ...
;         for (int t = 0; t < nt; t += 2) {
;             const bool last = (t == nt - 2);
;             const char* a1 = cA + (size_t)(t + 1) * kstep;
;             const char* a2 = last ? nA : cA + (size_t)(t + 2) * kstep; const char* b2 = last ? nB : cB + (size_t)(t + 2) * kstep;
;             const char* a3 = a2 + kstep; const char* b3 = b2 + kstep;
;             PG8_LDB(B0, 0, 0); PG8_LDB(B1, 0, 1); PG8_SCHED; PG8_LDA(At, 0, 0); PG8_STAGE_A(PG8_SA(1, 1), a1, 1, false);
;             PG8_WAIT_V(8); PG8_WAIT_L(0); PG8_BAR; PG8_MMA(0, 0, At, B0); PG8_MMA(0, 1, At, B1); PG8_BAR; PG8_SCHED;
;             PG8_LDA(At, 0, 1); PG8_STAGE(PG8_SB(0, 0), b2, voffB); PG8_STAGE(PG8_SB(0, 1), b2 + hstep, voffB); PG8_STAGE_A(PG8_SA(0, 0), a2, 0, last);
;             PG8_WAIT_V(8); PG8_WAIT_L(0); PG8_BAR; PG8_MMA(1, 0, At, B0); PG8_MMA(1, 1, At, B1); PG8_BAR; PG8_SCHED;
;             PG8_LDB(B0, 1, 0); PG8_LDB(B1, 1, 1); PG8_SCHED; PG8_LDA(At, 1, 0); PG8_STAGE_A(PG8_SA(0, 1), a2, 1, last);
;             PG8_WAIT_V(8); PG8_WAIT_L(0); PG8_BAR; PG8_MMA(0, 0, At, B0); PG8_MMA(0, 1, At, B1); PG8_BAR; PG8_SCHED;
;             PG8_LDA(At, 1, 1); PG8_STAGE(PG8_SB(1, 0), b3, voffB); PG8_STAGE(PG8_SB(1, 1), b3 + hstep, voffB); PG8_STAGE_A(PG8_SA(1, 0), a3, 0, last);
;             PG8_WAIT_V(8); PG8_WAIT_L(0); PG8_BAR; PG8_MMA(1, 0, At, B0); PG8_MMA(1, 1, At, B1); PG8_BAR; PG8_SCHED;
	s_add_i32 s34, s60, s40
	v_lshl_add_u64 v[148:149], v[148:149], 0, s[6:7]
	s_mov_b32 m0, s34
	ds_read_b128 v[192:195], v155 offset:49152
	ds_read_b128 v[196:199], v155 offset:50176
	ds_read_b128 v[200:203], v155 offset:51200
	ds_read_b128 v[204:207], v155 offset:52224
	ds_read_b128 v[208:211], v155 offset:53248
	ds_read_b128 v[212:215], v155 offset:54272
	ds_read_b128 v[216:219], v155 offset:55296
	ds_read_b128 v[220:223], v155 offset:56320
	global_load_lds_dwordx4 v[148:149], off
	s_add_i32 m0, s34, 0x2000
	s_add_u32 s30, s30, 0x20080
	v_lshl_add_u64 v[148:149], v[168:169], 0, s[6:7]
	s_addc_u32 s31, s31, 0
	s_add_i32 s34, s61, s40
	global_load_lds_dwordx4 v[148:149], off
	v_lshl_add_u64 v[148:149], s[30:31], 0, v[134:135]
	s_mov_b32 m0, s34
	s_nop 0
	global_load_lds_dwordx4 v[148:149], off
	v_lshl_add_u64 v[148:149], s[30:31], 0, v[138:139]
	s_add_i32 m0, s34, 0x2000
	s_nop 0
	global_load_lds_dwordx4 v[148:149], off
	v_lshl_add_u64 v[148:149], v[224:225], 0, s[6:7]
	s_mov_b32 m0, s45
	s_nop 0
	global_load_lds_dwordx4 v[148:149], off
	v_lshl_add_u64 v[148:149], v[226:227], 0, s[6:7]
	s_mov_b32 m0, s46
	s_nop 0
	global_load_lds_dwordx4 v[148:149], off
	s_waitcnt vmcnt(8)
	s_waitcnt lgkmcnt(0)
	s_barrier
	s_setprio 1
	s_waitcnt lgkmcnt(0)
	v_mfma_f32_16x16x32_bf16 v[62:65], v[156:159], v[192:195], v[62:65]
	v_mfma_f32_16x16x32_bf16 v[58:61], v[164:167], v[192:195], v[58:61]
	v_mfma_f32_16x16x32_bf16 v[54:57], v[156:159], v[200:203], v[54:57]
	v_mfma_f32_16x16x32_bf16 v[46:49], v[164:167], v[200:203], v[46:49]
	v_mfma_f32_16x16x32_bf16 v[38:41], v[156:159], v[208:211], v[38:41]
	v_mfma_f32_16x16x32_bf16 v[30:33], v[164:167], v[208:211], v[30:33]
	v_mfma_f32_16x16x32_bf16 v[22:25], v[156:159], v[216:219], v[22:25]
	v_mfma_f32_16x16x32_bf16 v[14:17], v[164:167], v[216:219], v[14:17]
	v_mfma_f32_16x16x32_bf16 v[62:65], v[160:163], v[196:199], v[62:65]
	v_mfma_f32_16x16x32_bf16 v[58:61], v[172:175], v[196:199], v[58:61]
	v_mfma_f32_16x16x32_bf16 v[54:57], v[160:163], v[204:207], v[54:57]
	v_mfma_f32_16x16x32_bf16 v[46:49], v[172:175], v[204:207], v[46:49]
	v_mfma_f32_16x16x32_bf16 v[38:41], v[160:163], v[212:215], v[38:41]
	v_mfma_f32_16x16x32_bf16 v[30:33], v[172:175], v[212:215], v[30:33]
	v_mfma_f32_16x16x32_bf16 v[22:25], v[160:163], v[220:223], v[22:25]
	v_mfma_f32_16x16x32_bf16 v[14:17], v[172:175], v[220:223], v[14:17]
	s_setprio 0
	s_setprio 1
	v_mfma_f32_16x16x32_bf16 v[50:53], v[176:179], v[192:195], v[50:53]
	v_mfma_f32_16x16x32_bf16 v[42:45], v[184:187], v[192:195], v[42:45]
	v_mfma_f32_16x16x32_bf16 v[34:37], v[176:179], v[200:203], v[34:37]
	v_mfma_f32_16x16x32_bf16 v[26:29], v[184:187], v[200:203], v[26:29]
	v_mfma_f32_16x16x32_bf16 v[18:21], v[176:179], v[208:211], v[18:21]
	v_mfma_f32_16x16x32_bf16 v[10:13], v[184:187], v[208:211], v[10:13]
	v_mfma_f32_16x16x32_bf16 v[6:9], v[176:179], v[216:219], v[6:9]
	v_mfma_f32_16x16x32_bf16 v[2:5], v[184:187], v[216:219], v[2:5]
	v_mfma_f32_16x16x32_bf16 v[50:53], v[180:183], v[196:199], v[50:53]
	v_mfma_f32_16x16x32_bf16 v[42:45], v[188:191], v[196:199], v[42:45]
	v_mfma_f32_16x16x32_bf16 v[34:37], v[180:183], v[204:207], v[34:37]
	v_mfma_f32_16x16x32_bf16 v[26:29], v[188:191], v[204:207], v[26:29]
	v_mfma_f32_16x16x32_bf16 v[18:21], v[180:183], v[212:215], v[18:21]
	v_mfma_f32_16x16x32_bf16 v[10:13], v[188:191], v[212:215], v[10:13]
	v_mfma_f32_16x16x32_bf16 v[6:9], v[180:183], v[220:223], v[6:9]
	v_mfma_f32_16x16x32_bf16 v[2:5], v[188:191], v[220:223], v[2:5]
	s_setprio 0
	s_add_i32 s59, s59, 2
	s_add_u32 s28, s28, 0x100
	s_addc_u32 s29, s29, 0
	s_add_u32 s57, s57, 0x100
	s_addc_u32 s58, s58, 0
	s_cmp_gt_u32 s59, 5
	s_barrier
	s_cbranch_scc0 .LBB0_335
	s_and_b64 vcc, exec, s[8:9]
	s_cbranch_vccz .LBB0_338
	s_barrier

; #define PG8_STAGE(bufoff, gbase, voff) do { _Pragma("unroll") for (int _i = 0; _i < 2; ++_i) \
;         __builtin_amdgcn_global_load_lds((const unsigned*)((const char*)(gbase) + (voff)[_i]), (LAS unsigned*)(lds + (bufoff) + ldsw + _i * 8192), 16, 0, 0); } while (0)
; #define PG8_LDA(dst, b, h) do { if constexpr (FP8) { _Pragma("unroll") for (int m = 0; m < 4; ++m) dst##8[m] = PG8_LD8(lds + PG8_SA(b, h) + aoff + m * 2048); } \
;         else { _Pragma("unroll") for (int m = 0; m < 4; ++m) _Pragma("unroll") for (int k = 0; k < 2; ++k) dst[m][k] = *(const LAS bf16x8*)(lds + PG8_SA(b, h) + aoff + m * 2048 + k * 1024); } } while (0)
; #define PG8_WAIT_V(n) asm volatile("s_waitcnt vmcnt(" #n ")" ::: "memory")
; #define PG8_WAIT_L(n) asm volatile("s_waitcnt lgkmcnt(" #n ")" ::: "memory")
; template <class Epi, class Sched, bool GATHER, bool FP8 = false>
; __device__ __forceinline__ void gemm_phase(LAS unsigned char* lds, const Gemm g, const Sched& S, const Epi& E) {
;     ...
;         for (int t = 0; t < nt; t += 2) {
;             const bool last = (t == nt - 2);
;             const char* a1 = cA + (size_t)(t + 1) * kstep;
;             const char* a2 = last ? nA : cA + (size_t)(t + 2) * kstep; const char* b2 = last ? nB : cB + (size_t)(t + 2) * kstep;
;             const char* a3 = a2 + kstep; const char* b3 = b2 + kstep;
;             PG8_LDB(B0, 0, 0); PG8_LDB(B1, 0, 1); PG8_SCHED; PG8_LDA(At, 0, 0); PG8_STAGE_A(PG8_SA(1, 1), a1, 1, false);
;             PG8_WAIT_V(8); PG8_WAIT_L(0); PG8_BAR; PG8_MMA(0, 0, At, B0); PG8_MMA(0, 1, At, B1); PG8_BAR; PG8_SCHED;
;             PG8_LDA(At, 0, 1); PG8_STAGE(PG8_SB(0, 0), b2, voffB); PG8_STAGE(PG8_SB(0, 1), b2 + hstep, voffB); PG8_STAGE_A(PG8_SA(0, 0), a2, 0, last);
;             PG8_WAIT_V(8); PG8_WAIT_L(0); PG8_BAR; PG8_MMA(1, 0, At, B0); PG8_MMA(1, 1, At, B1); PG8_BAR; PG8_SCHED;
;             PG8_LDB(B0, 1, 0); PG8_LDB(B1, 1, 1); PG8_SCHED; PG8_LDA(At, 1, 0); PG8_STAGE_A(PG8_SA(0, 1), a2, 1, last);
;             PG8_WAIT_V(8); PG8_WAIT_L(0); PG8_BAR; PG8_MMA(0, 0, At, B0); PG8_MMA(0, 1, At, B1); PG8_BAR; PG8_SCHED;
;             PG8_LDA(At, 1, 1); PG8_STAGE(PG8_SB(1, 0), b3, voffB); PG8_STAGE(PG8_SB(1, 1), b3 + hstep, voffB); PG8_STAGE_A(PG8_SA(1, 0), a3, 0, last);
;             PG8_WAIT_V(8); PG8_WAIT_L(0); PG8_BAR; PG8_MMA(1, 0, At, B0); PG8_MMA(1, 1, At, B1); PG8_BAR; PG8_SCHED;
.LBB0_1137:
	ds_read_b128 v[146:149], v154
	ds_read_b128 v[158:161], v154 offset:1024
	ds_read_b128 v[162:165], v154 offset:2048
	ds_read_b128 v[166:169], v154 offset:3072
	ds_read_b128 v[172:175], v155
	ds_read_b128 v[176:179], v155 offset:1024
	ds_read_b128 v[180:183], v155 offset:2048
	ds_read_b128 v[184:187], v155 offset:3072
	s_add_u32 s30, s28, 0xfff80080
	s_addc_u32 s31, s29, -1
	s_cmp_eq_u32 s55, 28
	s_cselect_b32 s35, s21, s31
	s_cselect_b32 s34, s51, s30
	s_cselect_b32 s31, s19, s54
	s_cselect_b32 s30, s52, s53
	v_lshl_add_u64 v[150:151], s[28:29], 0, v[138:139]
	s_add_i32 m0, s27, 0xc000
	ds_read_b128 v[188:191], v156
	ds_read_b128 v[192:195], v156 offset:1024
	ds_read_b128 v[196:199], v156 offset:2048
	ds_read_b128 v[200:203], v156 offset:3072
	ds_read_b128 v[204:207], v156 offset:4096
	ds_read_b128 v[208:211], v156 offset:5120
	ds_read_b128 v[212:215], v156 offset:6144
	ds_read_b128 v[216:219], v156 offset:7168
	global_load_lds_dwordx4 v[150:151], off
	v_lshl_add_u64 v[150:151], s[28:29], 0, v[140:141]
	s_add_i32 m0, s27, 0xe000
	s_nop 0
	global_load_lds_dwordx4 v[150:151], off
	s_waitcnt vmcnt(8)
	s_waitcnt lgkmcnt(0)
	s_barrier
	s_setprio 1
	s_waitcnt lgkmcnt(0)
	v_mfma_f32_16x16x32_bf16 v[126:129], v[146:149], v[188:191], v[126:129]
	v_mfma_f32_16x16x32_bf16 v[122:125], v[162:165], v[188:191], v[122:125]
	v_mfma_f32_16x16x32_bf16 v[110:113], v[146:149], v[196:199], v[110:113]
	v_mfma_f32_16x16x32_bf16 v[106:109], v[162:165], v[196:199], v[106:109]
	v_mfma_f32_16x16x32_bf16 v[94:97], v[146:149], v[204:207], v[94:97]
	v_mfma_f32_16x16x32_bf16 v[90:93], v[162:165], v[204:207], v[90:93]
	v_mfma_f32_16x16x32_bf16 v[78:81], v[146:149], v[212:215], v[78:81]
	v_mfma_f32_16x16x32_bf16 v[74:77], v[162:165], v[212:215], v[74:77]
	v_mfma_f32_16x16x32_bf16 v[126:129], v[158:161], v[192:195], v[126:129]
	v_mfma_f32_16x16x32_bf16 v[122:125], v[166:169], v[192:195], v[122:125]
	v_mfma_f32_16x16x32_bf16 v[110:113], v[158:161], v[200:203], v[110:113]
	v_mfma_f32_16x16x32_bf16 v[106:109], v[166:169], v[200:203], v[106:109]
	v_mfma_f32_16x16x32_bf16 v[94:97], v[158:161], v[208:211], v[94:97]
	v_mfma_f32_16x16x32_bf16 v[90:93], v[166:169], v[208:211], v[90:93]
	v_mfma_f32_16x16x32_bf16 v[78:81], v[158:161], v[216:219], v[78:81]
	v_mfma_f32_16x16x32_bf16 v[74:77], v[166:169], v[216:219], v[74:77]
	s_setprio 0
	s_setprio 1
	v_mfma_f32_16x16x32_bf16 v[118:121], v[172:175], v[188:191], v[118:121]
	v_mfma_f32_16x16x32_bf16 v[114:117], v[180:183], v[188:191], v[114:117]
	v_mfma_f32_16x16x32_bf16 v[102:105], v[172:175], v[196:199], v[102:105]
	v_mfma_f32_16x16x32_bf16 v[98:101], v[180:183], v[196:199], v[98:101]
	v_mfma_f32_16x16x32_bf16 v[86:89], v[172:175], v[204:207], v[86:89]
	v_mfma_f32_16x16x32_bf16 v[82:85], v[180:183], v[204:207], v[82:85]
	v_mfma_f32_16x16x32_bf16 v[70:73], v[172:175], v[212:215], v[70:73]
	v_mfma_f32_16x16x32_bf16 v[66:69], v[180:183], v[212:215], v[66:69]
	v_mfma_f32_16x16x32_bf16 v[118:121], v[176:179], v[192:195], v[118:121]
	v_mfma_f32_16x16x32_bf16 v[114:117], v[184:187], v[192:195], v[114:117]
	v_mfma_f32_16x16x32_bf16 v[102:105], v[176:179], v[200:203], v[102:105]
	v_mfma_f32_16x16x32_bf16 v[98:101], v[184:187], v[200:203], v[98:101]
	v_mfma_f32_16x16x32_bf16 v[86:89], v[176:179], v[208:211], v[86:89]
	v_mfma_f32_16x16x32_bf16 v[82:85], v[184:187], v[208:211], v[82:85]
	v_mfma_f32_16x16x32_bf16 v[70:73], v[176:179], v[216:219], v[70:73]
	v_mfma_f32_16x16x32_bf16 v[66:69], v[184:187], v[216:219], v[66:69]
	s_setprio 0
	s_barrier
	s_add_i32 s56, s48, s40
	v_lshl_add_u64 v[150:151], s[30:31], 0, v[132:133]
	s_mov_b32 m0, s56
	ds_read_b128 v[188:191], v156 offset:16384
	ds_read_b128 v[192:195], v156 offset:17408
	ds_read_b128 v[196:199], v156 offset:18432
	ds_read_b128 v[200:203], v156 offset:19456
	ds_read_b128 v[204:207], v156 offset:20480
	ds_read_b128 v[208:211], v156 offset:21504
	ds_read_b128 v[212:215], v156 offset:22528
	ds_read_b128 v[216:219], v156 offset:23552
	global_load_lds_dwordx4 v[150:151], off
	s_add_i32 m0, s56, 0x2000
	s_add_u32 s56, s30, 0x80000
	v_lshl_add_u64 v[220:221], s[30:31], 0, v[136:137]
	s_addc_u32 s57, s31, 0
	s_add_i32 s58, s49, s40
	global_load_lds_dwordx4 v[220:221], off
	v_lshl_add_u64 v[222:223], s[56:57], 0, v[132:133]
	s_mov_b32 m0, s58
	v_lshl_add_u64 v[224:225], s[34:35], 0, v[134:135]
	global_load_lds_dwordx4 v[222:223], off
	v_lshl_add_u64 v[222:223], s[56:57], 0, v[136:137]
	s_add_i32 m0, s58, 0x2000
	s_nop 0
	global_load_lds_dwordx4 v[222:223], off
	v_lshl_add_u64 v[222:223], s[34:35], 0, v[130:131]
	s_mov_b32 m0, s27
	s_nop 0
	global_load_lds_dwordx4 v[222:223], off
	s_mov_b32 m0, s41
	s_nop 0
	global_load_lds_dwordx4 v[224:225], off
	s_waitcnt vmcnt(8)
	s_waitcnt lgkmcnt(0)
	s_barrier
; #define PG8_STAGE(bufoff, gbase, voff) do { _Pragma("unroll") for (int _i = 0; _i < 2; ++_i) \
;         __builtin_amdgcn_global_load_lds((const unsigned*)((const char*)(gbase) + (voff)[_i]), (LAS unsigned*)(lds + (bufoff) + ldsw + _i * 8192), 16, 0, 0); } while (0)
; #define PG8_LDA(dst, b, h) do { if constexpr (FP8) { _Pragma("unroll") for (int m = 0; m < 4; ++m) dst##8[m] = PG8_LD8(lds + PG8_SA(b, h) + aoff + m * 2048); } \
;         else { _Pragma("unroll") for (int m = 0; m < 4; ++m) _Pragma("unroll") for (int k = 0; k < 2; ++k) dst[m][k] = *(const LAS bf16x8*)(lds + PG8_SA(b, h) + aoff + m * 2048 + k * 1024); } } while (0)
; #define PG8_WAIT_V(n) asm volatile("s_waitcnt vmcnt(" #n ")" ::: "memory")
; #define PG8_WAIT_L(n) asm volatile("s_waitcnt lgkmcnt(" #n ")" ::: "memory")
; template <class Epi, class Sched, bool GATHER, bool FP8 = false>
; __device__ __forceinline__ void gemm_phase(LAS unsigned char* lds, const Gemm g, const Sched& S, const Epi& E) {
;     ...
;         for (int t = 0; t < nt; t += 2) {
;             const bool last = (t == nt - 2);
;             const char* a1 = cA + (size_t)(t + 1) * kstep;
;             const char* a2 = last ? nA : cA + (size_t)(t + 2) * kstep; const char* b2 = last ? nB : cB + (size_t)(t + 2) * kstep;
;             const char* a3 = a2 + kstep; const char* b3 = b2 + kstep;
;             PG8_LDB(B0, 0, 0); PG8_LDB(B1, 0, 1); PG8_SCHED; PG8_LDA(At, 0, 0); PG8_STAGE_A(PG8_SA(1, 1), a1, 1, false);
;             PG8_WAIT_V(8); PG8_WAIT_L(0); PG8_BAR; PG8_MMA(0, 0, At, B0); PG8_MMA(0, 1, At, B1); PG8_BAR; PG8_SCHED;
;             PG8_LDA(At, 0, 1); PG8_STAGE(PG8_SB(0, 0), b2, voffB); PG8_STAGE(PG8_SB(0, 1), b2 + hstep, voffB); PG8_STAGE_A(PG8_SA(0, 0), a2, 0, last);
;             PG8_WAIT_V(8); PG8_WAIT_L(0); PG8_BAR; PG8_MMA(1, 0, At, B0); PG8_MMA(1, 1, At, B1); PG8_BAR; PG8_SCHED;
;             PG8_LDB(B0, 1, 0); PG8_LDB(B1, 1, 1); PG8_SCHED; PG8_LDA(At, 1, 0); PG8_STAGE_A(PG8_SA(0, 1), a2, 1, last);
;             PG8_WAIT_V(8); PG8_WAIT_L(0); PG8_BAR; PG8_MMA(0, 0, At, B0); PG8_MMA(0, 1, At, B1); PG8_BAR; PG8_SCHED;
;             PG8_LDA(At, 1, 1); PG8_STAGE(PG8_SB(1, 0), b3, voffB); PG8_STAGE(PG8_SB(1, 1), b3 + hstep, voffB); PG8_STAGE_A(PG8_SA(1, 0), a3, 0, last);
;             PG8_WAIT_V(8); PG8_WAIT_L(0); PG8_BAR; PG8_MMA(1, 0, At, B0); PG8_MMA(1, 1, At, B1); PG8_BAR; PG8_SCHED;
	s_setprio 1
	s_waitcnt lgkmcnt(0)
	v_mfma_f32_16x16x32_bf16 v[62:65], v[146:149], v[188:191], v[62:65]
	v_mfma_f32_16x16x32_bf16 v[58:61], v[162:165], v[188:191], v[58:61]
	v_mfma_f32_16x16x32_bf16 v[46:49], v[146:149], v[196:199], v[46:49]
	v_mfma_f32_16x16x32_bf16 v[42:45], v[162:165], v[196:199], v[42:45]
	v_mfma_f32_16x16x32_bf16 v[30:33], v[146:149], v[204:207], v[30:33]
	v_mfma_f32_16x16x32_bf16 v[26:29], v[162:165], v[204:207], v[26:29]
	v_mfma_f32_16x16x32_bf16 v[14:17], v[146:149], v[212:215], v[14:17]
	v_mfma_f32_16x16x32_bf16 v[10:13], v[162:165], v[212:215], v[10:13]
	v_mfma_f32_16x16x32_bf16 v[62:65], v[158:161], v[192:195], v[62:65]
	v_mfma_f32_16x16x32_bf16 v[58:61], v[166:169], v[192:195], v[58:61]
	v_mfma_f32_16x16x32_bf16 v[46:49], v[158:161], v[200:203], v[46:49]
	v_mfma_f32_16x16x32_bf16 v[42:45], v[166:169], v[200:203], v[42:45]
	v_mfma_f32_16x16x32_bf16 v[30:33], v[158:161], v[208:211], v[30:33]
	v_mfma_f32_16x16x32_bf16 v[26:29], v[166:169], v[208:211], v[26:29]
	v_mfma_f32_16x16x32_bf16 v[14:17], v[158:161], v[216:219], v[14:17]
	v_mfma_f32_16x16x32_bf16 v[10:13], v[166:169], v[216:219], v[10:13]
	s_setprio 0
	s_setprio 1
	v_mfma_f32_16x16x32_bf16 v[54:57], v[172:175], v[188:191], v[54:57]
	v_mfma_f32_16x16x32_bf16 v[50:53], v[180:183], v[188:191], v[50:53]
	v_mfma_f32_16x16x32_bf16 v[38:41], v[172:175], v[196:199], v[38:41]
	v_mfma_f32_16x16x32_bf16 v[34:37], v[180:183], v[196:199], v[34:37]
	v_mfma_f32_16x16x32_bf16 v[22:25], v[172:175], v[204:207], v[22:25]
	v_mfma_f32_16x16x32_bf16 v[18:21], v[180:183], v[204:207], v[18:21]
	v_mfma_f32_16x16x32_bf16 v[6:9], v[172:175], v[212:215], v[6:9]
	v_mfma_f32_16x16x32_bf16 v[2:5], v[180:183], v[212:215], v[2:5]
	v_mfma_f32_16x16x32_bf16 v[54:57], v[176:179], v[192:195], v[54:57]
	v_mfma_f32_16x16x32_bf16 v[50:53], v[184:187], v[192:195], v[50:53]
	v_mfma_f32_16x16x32_bf16 v[38:41], v[176:179], v[200:203], v[38:41]
	v_mfma_f32_16x16x32_bf16 v[34:37], v[184:187], v[200:203], v[34:37]
	v_mfma_f32_16x16x32_bf16 v[22:25], v[176:179], v[208:211], v[22:25]
	v_mfma_f32_16x16x32_bf16 v[18:21], v[184:187], v[208:211], v[18:21]
	v_mfma_f32_16x16x32_bf16 v[6:9], v[176:179], v[216:219], v[6:9]
	v_mfma_f32_16x16x32_bf16 v[2:5], v[184:187], v[216:219], v[2:5]
	s_setprio 0
	s_barrier
	s_add_i32 s56, 0, 0x18000
	v_add_u32_e32 v157, s56, v152
	s_add_i32 s57, 0, 0x1c000
	ds_read_b128 v[146:149], v157
	ds_read_b128 v[158:161], v157 offset:1024
	ds_read_b128 v[162:165], v157 offset:2048
	ds_read_b128 v[166:169], v157 offset:3072
	v_add_u32_e32 v157, s57, v152
	ds_read_b128 v[172:175], v157
	ds_read_b128 v[176:179], v157 offset:1024
	ds_read_b128 v[180:183], v157 offset:2048
	ds_read_b128 v[184:187], v157 offset:3072
	s_add_u32 s34, s34, 0x80000
	s_addc_u32 s35, s35, 0
	s_mov_b32 m0, s42
	v_lshl_add_u64 v[226:227], s[34:35], 0, v[130:131]
	ds_read_b128 v[188:191], v156 offset:32768
	ds_read_b128 v[192:195], v156 offset:33792
	ds_read_b128 v[196:199], v156 offset:34816
	ds_read_b128 v[200:203], v156 offset:35840
	ds_read_b128 v[204:207], v156 offset:36864
	ds_read_b128 v[208:211], v156 offset:37888
	ds_read_b128 v[212:215], v156 offset:38912
	ds_read_b128 v[216:219], v156 offset:39936
	global_load_lds_dwordx4 v[226:227], off
	v_lshl_add_u64 v[226:227], s[34:35], 0, v[134:135]
	s_mov_b32 m0, s43
	s_nop 0
	global_load_lds_dwordx4 v[226:227], off
	s_waitcnt vmcnt(8)
	s_waitcnt lgkmcnt(0)
	s_barrier
	s_setprio 1
	s_waitcnt lgkmcnt(0)
	v_mfma_f32_16x16x32_bf16 v[126:129], v[146:149], v[188:191], v[126:129]
	v_mfma_f32_16x16x32_bf16 v[122:125], v[162:165], v[188:191], v[122:125]
	v_mfma_f32_16x16x32_bf16 v[110:113], v[146:149], v[196:199], v[110:113]
	v_mfma_f32_16x16x32_bf16 v[106:109], v[162:165], v[196:199], v[106:109]
	v_mfma_f32_16x16x32_bf16 v[94:97], v[146:149], v[204:207], v[94:97]
	v_mfma_f32_16x16x32_bf16 v[90:93], v[162:165], v[204:207], v[90:93]
	v_mfma_f32_16x16x32_bf16 v[78:81], v[146:149], v[212:215], v[78:81]
	v_mfma_f32_16x16x32_bf16 v[74:77], v[162:165], v[212:215], v[74:77]
	v_mfma_f32_16x16x32_bf16 v[126:129], v[158:161], v[192:195], v[126:129]
	v_mfma_f32_16x16x32_bf16 v[122:125], v[166:169], v[192:195], v[122:125]
	v_mfma_f32_16x16x32_bf16 v[110:113], v[158:161], v[200:203], v[110:113]
	v_mfma_f32_16x16x32_bf16 v[106:109], v[166:169], v[200:203], v[106:109]
	v_mfma_f32_16x16x32_bf16 v[94:97], v[158:161], v[208:211], v[94:97]
	v_mfma_f32_16x16x32_bf16 v[90:93], v[166:169], v[208:211], v[90:93]
	v_mfma_f32_16x16x32_bf16 v[78:81], v[158:161], v[216:219], v[78:81]
	v_mfma_f32_16x16x32_bf16 v[74:77], v[166:169], v[216:219], v[74:77]
	s_setprio 0
	s_setprio 1
	v_mfma_f32_16x16x32_bf16 v[118:121], v[172:175], v[188:191], v[118:121]
	v_mfma_f32_16x16x32_bf16 v[114:117], v[180:183], v[188:191], v[114:117]
	v_mfma_f32_16x16x32_bf16 v[102:105], v[172:175], v[196:199], v[102:105]
	v_mfma_f32_16x16x32_bf16 v[98:101], v[180:183], v[196:199], v[98:101]
	v_mfma_f32_16x16x32_bf16 v[86:89], v[172:175], v[204:207], v[86:89]
	v_mfma_f32_16x16x32_bf16 v[82:85], v[180:183], v[204:207], v[82:85]
	v_mfma_f32_16x16x32_bf16 v[70:73], v[172:175], v[212:215], v[70:73]
	v_mfma_f32_16x16x32_bf16 v[66:69], v[180:183], v[212:215], v[66:69]
	v_mfma_f32_16x16x32_bf16 v[118:121], v[176:179], v[192:195], v[118:121]
	v_mfma_f32_16x16x32_bf16 v[114:117], v[184:187], v[192:195], v[114:117]
	v_mfma_f32_16x16x32_bf16 v[102:105], v[176:179], v[200:203], v[102:105]
	v_mfma_f32_16x16x32_bf16 v[98:101], v[184:187], v[200:203], v[98:101]
	v_mfma_f32_16x16x32_bf16 v[86:89], v[176:179], v[208:211], v[86:89]
	v_mfma_f32_16x16x32_bf16 v[82:85], v[184:187], v[208:211], v[82:85]
	v_mfma_f32_16x16x32_bf16 v[70:73], v[176:179], v[216:219], v[70:73]
	v_mfma_f32_16x16x32_bf16 v[66:69], v[184:187], v[216:219], v[66:69]
	s_setprio 0
	s_barrier
; #define PG8_STAGE(bufoff, gbase, voff) do { _Pragma("unroll") for (int _i = 0; _i < 2; ++_i) \
;         __builtin_amdgcn_global_load_lds((const unsigned*)((const char*)(gbase) + (voff)[_i]), (LAS unsigned*)(lds + (bufoff) + ldsw + _i * 8192), 16, 0, 0); } while (0)
; #define PG8_LDA(dst, b, h) do { if constexpr (FP8) { _Pragma("unroll") for (int m = 0; m < 4; ++m) dst##8[m] = PG8_LD8(lds + PG8_SA(b, h) + aoff + m * 2048); } \
;         else { _Pragma("unroll") for (int m = 0; m < 4; ++m) _Pragma("unroll") for (int k = 0; k < 2; ++k) dst[m][k] = *(const LAS bf16x8*)(lds + PG8_SA(b, h) + aoff + m * 2048 + k * 1024); } } while (0)
; #define PG8_WAIT_V(n) asm volatile("s_waitcnt vmcnt(" #n ")" ::: "memory")
; #define PG8_WAIT_L(n) asm volatile("s_waitcnt lgkmcnt(" #n ")" ::: "memory")
; template <class Epi, class Sched, bool GATHER, bool FP8 = false>
; __device__ __forceinline__ void gemm_phase(LAS unsigned char* lds, const Gemm g, const Sched& S, const Epi& E) {
;     ...
;         for (int t = 0; t < nt; t += 2) {
;             const bool last = (t == nt - 2);
;             const char* a1 = cA + (size_t)(t + 1) * kstep;
;             const char* a2 = last ? nA : cA + (size_t)(t + 2) * kstep; const char* b2 = last ? nB : cB + (size_t)(t + 2) * kstep;
;             const char* a3 = a2 + kstep; const char* b3 = b2 + kstep;
;             PG8_LDB(B0, 0, 0); PG8_LDB(B1, 0, 1); PG8_SCHED; PG8_LDA(At, 0, 0); PG8_STAGE_A(PG8_SA(1, 1), a1, 1, false);
;             PG8_WAIT_V(8); PG8_WAIT_L(0); PG8_BAR; PG8_MMA(0, 0, At, B0); PG8_MMA(0, 1, At, B1); PG8_BAR; PG8_SCHED;
;             PG8_LDA(At, 0, 1); PG8_STAGE(PG8_SB(0, 0), b2, voffB); PG8_STAGE(PG8_SB(0, 1), b2 + hstep, voffB); PG8_STAGE_A(PG8_SA(0, 0), a2, 0, last);
;             PG8_WAIT_V(8); PG8_WAIT_L(0); PG8_BAR; PG8_MMA(1, 0, At, B0); PG8_MMA(1, 1, At, B1); PG8_BAR; PG8_SCHED;
;             PG8_LDB(B0, 1, 0); PG8_LDB(B1, 1, 1); PG8_SCHED; PG8_LDA(At, 1, 0); PG8_STAGE_A(PG8_SA(0, 1), a2, 1, last);
;             PG8_WAIT_V(8); PG8_WAIT_L(0); PG8_BAR; PG8_MMA(0, 0, At, B0); PG8_MMA(0, 1, At, B1); PG8_BAR; PG8_SCHED;
;             PG8_LDA(At, 1, 1); PG8_STAGE(PG8_SB(1, 0), b3, voffB); PG8_STAGE(PG8_SB(1, 1), b3 + hstep, voffB); PG8_STAGE_A(PG8_SA(1, 0), a3, 0, last);
;             PG8_WAIT_V(8); PG8_WAIT_L(0); PG8_BAR; PG8_MMA(1, 0, At, B0); PG8_MMA(1, 1, At, B1); PG8_BAR; PG8_SCHED;
	s_add_i32 s34, s56, s40
	v_lshl_add_u64 v[150:151], v[150:151], 0, s[6:7]
	s_mov_b32 m0, s34
	ds_read_b128 v[188:191], v156 offset:49152
	ds_read_b128 v[192:195], v156 offset:50176
	ds_read_b128 v[196:199], v156 offset:51200
	ds_read_b128 v[200:203], v156 offset:52224
	ds_read_b128 v[204:207], v156 offset:53248
	ds_read_b128 v[208:211], v156 offset:54272
	ds_read_b128 v[212:215], v156 offset:55296
	ds_read_b128 v[216:219], v156 offset:56320
	global_load_lds_dwordx4 v[150:151], off
	s_add_i32 m0, s34, 0x2000
	s_add_u32 s30, s30, 0x80080
	v_lshl_add_u64 v[150:151], v[220:221], 0, s[6:7]
	s_addc_u32 s31, s31, 0
	s_add_i32 s34, s57, s40
	global_load_lds_dwordx4 v[150:151], off
	v_lshl_add_u64 v[150:151], s[30:31], 0, v[132:133]
	s_mov_b32 m0, s34
	s_nop 0
	global_load_lds_dwordx4 v[150:151], off
	v_lshl_add_u64 v[150:151], s[30:31], 0, v[136:137]
	s_add_i32 m0, s34, 0x2000
	s_nop 0
	global_load_lds_dwordx4 v[150:151], off
	v_lshl_add_u64 v[150:151], v[222:223], 0, s[6:7]
	s_mov_b32 m0, s45
	s_nop 0
	global_load_lds_dwordx4 v[150:151], off
	v_lshl_add_u64 v[150:151], v[224:225], 0, s[6:7]
	s_mov_b32 m0, s46
	s_nop 0
	global_load_lds_dwordx4 v[150:151], off
	s_waitcnt vmcnt(8)
	s_waitcnt lgkmcnt(0)
	s_barrier
	s_setprio 1
	s_waitcnt lgkmcnt(0)
	v_mfma_f32_16x16x32_bf16 v[62:65], v[146:149], v[188:191], v[62:65]
	v_mfma_f32_16x16x32_bf16 v[58:61], v[162:165], v[188:191], v[58:61]
	v_mfma_f32_16x16x32_bf16 v[46:49], v[146:149], v[196:199], v[46:49]
	v_mfma_f32_16x16x32_bf16 v[42:45], v[162:165], v[196:199], v[42:45]
	v_mfma_f32_16x16x32_bf16 v[30:33], v[146:149], v[204:207], v[30:33]
	v_mfma_f32_16x16x32_bf16 v[26:29], v[162:165], v[204:207], v[26:29]
	v_mfma_f32_16x16x32_bf16 v[14:17], v[146:149], v[212:215], v[14:17]
	v_mfma_f32_16x16x32_bf16 v[10:13], v[162:165], v[212:215], v[10:13]
	v_mfma_f32_16x16x32_bf16 v[62:65], v[158:161], v[192:195], v[62:65]
	v_mfma_f32_16x16x32_bf16 v[58:61], v[166:169], v[192:195], v[58:61]
	v_mfma_f32_16x16x32_bf16 v[46:49], v[158:161], v[200:203], v[46:49]
	v_mfma_f32_16x16x32_bf16 v[42:45], v[166:169], v[200:203], v[42:45]
	v_mfma_f32_16x16x32_bf16 v[30:33], v[158:161], v[208:211], v[30:33]
	v_mfma_f32_16x16x32_bf16 v[26:29], v[166:169], v[208:211], v[26:29]
	v_mfma_f32_16x16x32_bf16 v[14:17], v[158:161], v[216:219], v[14:17]
	v_mfma_f32_16x16x32_bf16 v[10:13], v[166:169], v[216:219], v[10:13]
	s_setprio 0
	s_setprio 1
	v_mfma_f32_16x16x32_bf16 v[54:57], v[172:175], v[188:191], v[54:57]
	v_mfma_f32_16x16x32_bf16 v[50:53], v[180:183], v[188:191], v[50:53]
	v_mfma_f32_16x16x32_bf16 v[38:41], v[172:175], v[196:199], v[38:41]
	v_mfma_f32_16x16x32_bf16 v[34:37], v[180:183], v[196:199], v[34:37]
	v_mfma_f32_16x16x32_bf16 v[22:25], v[172:175], v[204:207], v[22:25]
	v_mfma_f32_16x16x32_bf16 v[18:21], v[180:183], v[204:207], v[18:21]
	v_mfma_f32_16x16x32_bf16 v[6:9], v[172:175], v[212:215], v[6:9]
	v_mfma_f32_16x16x32_bf16 v[2:5], v[180:183], v[212:215], v[2:5]
	v_mfma_f32_16x16x32_bf16 v[54:57], v[176:179], v[192:195], v[54:57]
	v_mfma_f32_16x16x32_bf16 v[50:53], v[184:187], v[192:195], v[50:53]
	v_mfma_f32_16x16x32_bf16 v[38:41], v[176:179], v[200:203], v[38:41]
	v_mfma_f32_16x16x32_bf16 v[34:37], v[184:187], v[200:203], v[34:37]
	v_mfma_f32_16x16x32_bf16 v[22:25], v[176:179], v[208:211], v[22:25]
	v_mfma_f32_16x16x32_bf16 v[18:21], v[184:187], v[208:211], v[18:21]
	v_mfma_f32_16x16x32_bf16 v[6:9], v[176:179], v[216:219], v[6:9]
	v_mfma_f32_16x16x32_bf16 v[2:5], v[184:187], v[216:219], v[2:5]
	s_setprio 0
	s_add_i32 s55, s55, 2
	s_add_u32 s28, s28, 0x100
	s_addc_u32 s29, s29, 0
	s_add_u32 s53, s53, 0x100
	s_addc_u32 s54, s54, 0
	s_cmp_gt_u32 s55, 29
	s_barrier
	s_cbranch_scc0 .LBB0_1137
	s_and_b64 vcc, exec, s[8:9]
	s_cbranch_vccz .LBB0_1140
	s_barrier

; #define PG8_STAGE(bufoff, gbase, voff) do { _Pragma("unroll") for (int _i = 0; _i < 2; ++_i) \
;         __builtin_amdgcn_global_load_lds((const unsigned*)((const char*)(gbase) + (voff)[_i]), (LAS unsigned*)(lds + (bufoff) + ldsw + _i * 8192), 16, 0, 0); } while (0)
; #define PG8_LDA(dst, b, h) do { if constexpr (FP8) { _Pragma("unroll") for (int m = 0; m < 4; ++m) dst##8[m] = PG8_LD8(lds + PG8_SA(b, h) + aoff + m * 2048); } \
;         else { _Pragma("unroll") for (int m = 0; m < 4; ++m) _Pragma("unroll") for (int k = 0; k < 2; ++k) dst[m][k] = *(const LAS bf16x8*)(lds + PG8_SA(b, h) + aoff + m * 2048 + k * 1024); } } while (0)
; #define PG8_WAIT_V(n) asm volatile("s_waitcnt vmcnt(" #n ")" ::: "memory")
; #define PG8_WAIT_L(n) asm volatile("s_waitcnt lgkmcnt(" #n ")" ::: "memory")
; template <class Epi, class Sched, bool GATHER, bool FP8 = false>
; __device__ __forceinline__ void gemm_phase(LAS unsigned char* lds, const Gemm g, const Sched& S, const Epi& E) {
;     ...
;         for (int t = 0; t < nt; t += 2) {
;             const bool last = (t == nt - 2);
;             const char* a1 = cA + (size_t)(t + 1) * kstep;
;             const char* a2 = last ? nA : cA + (size_t)(t + 2) * kstep; const char* b2 = last ? nB : cB + (size_t)(t + 2) * kstep;
;             const char* a3 = a2 + kstep; const char* b3 = b2 + kstep;
;             PG8_LDB(B0, 0, 0); PG8_LDB(B1, 0, 1); PG8_SCHED; PG8_LDA(At, 0, 0); PG8_STAGE_A(PG8_SA(1, 1), a1, 1, false);
;             PG8_WAIT_V(8); PG8_WAIT_L(0); PG8_BAR; PG8_MMA(0, 0, At, B0); PG8_MMA(0, 1, At, B1); PG8_BAR; PG8_SCHED;
;             PG8_LDA(At, 0, 1); PG8_STAGE(PG8_SB(0, 0), b2, voffB); PG8_STAGE(PG8_SB(0, 1), b2 + hstep, voffB); PG8_STAGE_A(PG8_SA(0, 0), a2, 0, last);
;             PG8_WAIT_V(8); PG8_WAIT_L(0); PG8_BAR; PG8_MMA(1, 0, At, B0); PG8_MMA(1, 1, At, B1); PG8_BAR; PG8_SCHED;
;             PG8_LDB(B0, 1, 0); PG8_LDB(B1, 1, 1); PG8_SCHED; PG8_LDA(At, 1, 0); PG8_STAGE_A(PG8_SA(0, 1), a2, 1, last);
;             PG8_WAIT_V(8); PG8_WAIT_L(0); PG8_BAR; PG8_MMA(0, 0, At, B0); PG8_MMA(0, 1, At, B1); PG8_BAR; PG8_SCHED;
;             PG8_LDA(At, 1, 1); PG8_STAGE(PG8_SB(1, 0), b3, voffB); PG8_STAGE(PG8_SB(1, 1), b3 + hstep, voffB); PG8_STAGE_A(PG8_SA(1, 0), a3, 0, last);
;             PG8_WAIT_V(8); PG8_WAIT_L(0); PG8_BAR; PG8_MMA(1, 0, At, B0); PG8_MMA(1, 1, At, B1); PG8_BAR; PG8_SCHED;
.LBB0_1428:
	ds_read_b128 v[18:21], v201
	ds_read_b128 v[22:25], v201 offset:1024
	ds_read_b128 v[26:29], v201 offset:2048
	ds_read_b128 v[30:33], v201 offset:3072
	ds_read_b128 v[2:5], v202
	ds_read_b128 v[6:9], v202 offset:1024
	ds_read_b128 v[10:13], v202 offset:2048
	ds_read_b128 v[14:17], v202 offset:3072
	s_add_u32 s26, s30, 0x100
	s_addc_u32 s27, s31, 0
	s_add_u32 s34, s23, s30
	s_addc_u32 s35, s25, s31
	s_cmpk_eq_i32 s30, 0x700
	s_cselect_b64 vcc, -1, 0
	s_and_b64 s[28:29], vcc, exec
	s_cselect_b32 s64, 0, s26
	s_cselect_b32 s63, 0, s27
	s_cselect_b32 s28, s2, s34
	s_cselect_b32 s29, s3, s35
	s_add_u32 s34, s6, s64
	s_addc_u32 s35, s7, s63
	v_lshl_add_u64 v[234:235], v[188:189], 0, s[30:31]
	s_add_i32 m0, s39, 0xc000
	ds_read_b128 v[190:193], v203
	ds_read_b128 v[194:197], v203 offset:1024
	ds_read_b128 v[210:213], v203 offset:2048
	ds_read_b128 v[214:217], v203 offset:3072
	ds_read_b128 v[218:221], v203 offset:4096
	ds_read_b128 v[222:225], v203 offset:5120
	ds_read_b128 v[226:229], v203 offset:6144
	ds_read_b128 v[230:233], v203 offset:7168
	global_load_lds_dwordx4 v[234:235], off
	v_lshl_add_u64 v[234:235], v[186:187], 0, s[30:31]
	s_add_i32 m0, s39, 0xe000
	s_nop 0
	global_load_lds_dwordx4 v[234:235], off
	s_waitcnt vmcnt(8)
	s_waitcnt lgkmcnt(0)
	s_barrier
	s_setprio 1
	s_waitcnt lgkmcnt(0)
	v_mfma_f32_16x16x128_f8f6f4 v[158:161], v[18:25], v[190:197], v[158:161]
	v_mfma_f32_16x16x128_f8f6f4 v[150:153], v[26:33], v[190:197], v[150:153]
	v_mfma_f32_16x16x128_f8f6f4 v[142:145], v[18:25], v[210:217], v[142:145]
	v_mfma_f32_16x16x128_f8f6f4 v[134:137], v[26:33], v[210:217], v[134:137]
	v_mfma_f32_16x16x128_f8f6f4 v[126:129], v[18:25], v[218:225], v[126:129]
	v_mfma_f32_16x16x128_f8f6f4 v[118:121], v[26:33], v[218:225], v[118:121]
	v_mfma_f32_16x16x128_f8f6f4 v[110:113], v[18:25], v[226:233], v[110:113]
	v_mfma_f32_16x16x128_f8f6f4 v[102:105], v[26:33], v[226:233], v[102:105]
	s_setprio 0
	s_setprio 1
	v_mfma_f32_16x16x128_f8f6f4 v[154:157], v[2:9], v[190:197], v[154:157]
	v_mfma_f32_16x16x128_f8f6f4 v[146:149], v[10:17], v[190:197], v[146:149]
	v_mfma_f32_16x16x128_f8f6f4 v[138:141], v[2:9], v[210:217], v[138:141]
	v_mfma_f32_16x16x128_f8f6f4 v[130:133], v[10:17], v[210:217], v[130:133]
	v_mfma_f32_16x16x128_f8f6f4 v[122:125], v[2:9], v[218:225], v[122:125]
	v_mfma_f32_16x16x128_f8f6f4 v[114:117], v[10:17], v[218:225], v[114:117]
	v_mfma_f32_16x16x128_f8f6f4 v[106:109], v[2:9], v[226:233], v[106:109]
	v_mfma_f32_16x16x128_f8f6f4 v[98:101], v[10:17], v[226:233], v[98:101]
	s_setprio 0
	s_barrier
	s_add_i32 s30, s52, s38
	v_lshl_add_u64 v[190:191], s[28:29], 0, v[168:169]
	s_mov_b32 m0, s30
	ds_read_b128 v[210:213], v203 offset:16384
	ds_read_b128 v[214:217], v203 offset:17408
	ds_read_b128 v[218:221], v203 offset:18432
	ds_read_b128 v[222:225], v203 offset:19456
	ds_read_b128 v[226:229], v203 offset:20480
	ds_read_b128 v[230:233], v203 offset:21504
	ds_read_b128 v[234:237], v203 offset:22528
	ds_read_b128 v[238:241], v203 offset:23552
	global_load_lds_dwordx4 v[190:191], off
	s_add_i32 m0, s30, 0x2000
	s_add_u32 s30, s28, 0x40000
	v_lshl_add_u64 v[192:193], s[28:29], 0, v[172:173]
	s_addc_u32 s31, s29, 0
	s_add_i32 s63, s53, s38
	global_load_lds_dwordx4 v[192:193], off
	v_lshl_add_u64 v[194:195], s[30:31], 0, v[168:169]
	s_mov_b32 m0, s63
	v_cndmask_b32_e32 v164, v209, v206, vcc
	global_load_lds_dwordx4 v[194:195], off
	v_lshl_add_u64 v[194:195], s[30:31], 0, v[172:173]
	s_add_i32 m0, s63, 0x2000
	s_nop 0
	global_load_lds_dwordx4 v[194:195], off
	v_lshl_add_u64 v[194:195], s[34:35], 0, v[164:165]
	v_cndmask_b32_e32 v164, v180, v205, vcc
	v_lshl_add_u64 v[194:195], v[194:195], 0, v[166:167]
	s_mov_b32 m0, s39
	v_lshl_add_u64 v[196:197], s[34:35], 0, v[164:165]
	global_load_lds_dwordx4 v[194:195], off
	v_lshl_add_u64 v[196:197], v[196:197], 0, v[166:167]
	s_mov_b32 m0, s40
	s_nop 0
	global_load_lds_dwordx4 v[196:197], off
	s_waitcnt vmcnt(8)
	s_waitcnt lgkmcnt(0)
	s_barrier
	s_setprio 1
	s_waitcnt lgkmcnt(0)
	v_mfma_f32_16x16x128_f8f6f4 v[94:97], v[18:25], v[210:217], v[94:97]
	v_mfma_f32_16x16x128_f8f6f4 v[86:89], v[26:33], v[210:217], v[86:89]
	v_mfma_f32_16x16x128_f8f6f4 v[78:81], v[18:25], v[218:225], v[78:81]
	v_mfma_f32_16x16x128_f8f6f4 v[70:73], v[26:33], v[218:225], v[70:73]
	v_mfma_f32_16x16x128_f8f6f4 v[62:65], v[18:25], v[226:233], v[62:65]
	v_mfma_f32_16x16x128_f8f6f4 v[54:57], v[26:33], v[226:233], v[54:57]
	v_mfma_f32_16x16x128_f8f6f4 v[46:49], v[18:25], v[234:241], v[46:49]
	v_mfma_f32_16x16x128_f8f6f4 v[38:41], v[26:33], v[234:241], v[38:41]
	s_setprio 0
	s_setprio 1
	v_mfma_f32_16x16x128_f8f6f4 v[90:93], v[2:9], v[210:217], v[90:93]
	v_mfma_f32_16x16x128_f8f6f4 v[82:85], v[10:17], v[210:217], v[82:85]
	v_mfma_f32_16x16x128_f8f6f4 v[74:77], v[2:9], v[218:225], v[74:77]
	v_mfma_f32_16x16x128_f8f6f4 v[66:69], v[10:17], v[218:225], v[66:69]
	v_mfma_f32_16x16x128_f8f6f4 v[58:61], v[2:9], v[226:233], v[58:61]
	v_mfma_f32_16x16x128_f8f6f4 v[50:53], v[10:17], v[226:233], v[50:53]
	v_mfma_f32_16x16x128_f8f6f4 v[42:45], v[2:9], v[234:241], v[42:45]
	v_mfma_f32_16x16x128_f8f6f4 v[34:37], v[10:17], v[234:241], v[34:37]
	s_setprio 0
	s_barrier
; #define PG8_STAGE(bufoff, gbase, voff) do { _Pragma("unroll") for (int _i = 0; _i < 2; ++_i) \
;         __builtin_amdgcn_global_load_lds((const unsigned*)((const char*)(gbase) + (voff)[_i]), (LAS unsigned*)(lds + (bufoff) + ldsw + _i * 8192), 16, 0, 0); } while (0)
; #define PG8_LDA(dst, b, h) do { if constexpr (FP8) { _Pragma("unroll") for (int m = 0; m < 4; ++m) dst##8[m] = PG8_LD8(lds + PG8_SA(b, h) + aoff + m * 2048); } \
;         else { _Pragma("unroll") for (int m = 0; m < 4; ++m) _Pragma("unroll") for (int k = 0; k < 2; ++k) dst[m][k] = *(const LAS bf16x8*)(lds + PG8_SA(b, h) + aoff + m * 2048 + k * 1024); } } while (0)
; #define PG8_WAIT_V(n) asm volatile("s_waitcnt vmcnt(" #n ")" ::: "memory")
; #define PG8_WAIT_L(n) asm volatile("s_waitcnt lgkmcnt(" #n ")" ::: "memory")
; template <class Epi, class Sched, bool GATHER, bool FP8 = false>
; __device__ __forceinline__ void gemm_phase(LAS unsigned char* lds, const Gemm g, const Sched& S, const Epi& E) {
;     ...
;         for (int t = 0; t < nt; t += 2) {
;             const bool last = (t == nt - 2);
;             const char* a1 = cA + (size_t)(t + 1) * kstep;
;             const char* a2 = last ? nA : cA + (size_t)(t + 2) * kstep; const char* b2 = last ? nB : cB + (size_t)(t + 2) * kstep;
;             const char* a3 = a2 + kstep; const char* b3 = b2 + kstep;
;             PG8_LDB(B0, 0, 0); PG8_LDB(B1, 0, 1); PG8_SCHED; PG8_LDA(At, 0, 0); PG8_STAGE_A(PG8_SA(1, 1), a1, 1, false);
;             PG8_WAIT_V(8); PG8_WAIT_L(0); PG8_BAR; PG8_MMA(0, 0, At, B0); PG8_MMA(0, 1, At, B1); PG8_BAR; PG8_SCHED;
;             PG8_LDA(At, 0, 1); PG8_STAGE(PG8_SB(0, 0), b2, voffB); PG8_STAGE(PG8_SB(0, 1), b2 + hstep, voffB); PG8_STAGE_A(PG8_SA(0, 0), a2, 0, last);
;             PG8_WAIT_V(8); PG8_WAIT_L(0); PG8_BAR; PG8_MMA(1, 0, At, B0); PG8_MMA(1, 1, At, B1); PG8_BAR; PG8_SCHED;
;             PG8_LDB(B0, 1, 0); PG8_LDB(B1, 1, 1); PG8_SCHED; PG8_LDA(At, 1, 0); PG8_STAGE_A(PG8_SA(0, 1), a2, 1, last);
;             PG8_WAIT_V(8); PG8_WAIT_L(0); PG8_BAR; PG8_MMA(0, 0, At, B0); PG8_MMA(0, 1, At, B1); PG8_BAR; PG8_SCHED;
;             PG8_LDA(At, 1, 1); PG8_STAGE(PG8_SB(1, 0), b3, voffB); PG8_STAGE(PG8_SB(1, 1), b3 + hstep, voffB); PG8_STAGE_A(PG8_SA(1, 0), a3, 0, last);
;             PG8_WAIT_V(8); PG8_WAIT_L(0); PG8_BAR; PG8_MMA(1, 0, At, B0); PG8_MMA(1, 1, At, B1); PG8_BAR; PG8_SCHED;
	s_add_i32 s30, 0, 0x18000
	s_add_i32 s31, 0, 0x1c000
	v_add_u32_e32 v14, s30, v200
	v_add_u32_e32 v30, s31, v200
	ds_read_b128 v[2:5], v14
	ds_read_b128 v[6:9], v14 offset:1024
	ds_read_b128 v[10:13], v14 offset:2048
	ds_read_b128 v[14:17], v14 offset:3072
	ds_read_b128 v[18:21], v30
	ds_read_b128 v[22:25], v30 offset:1024
	ds_read_b128 v[26:29], v30 offset:2048
	ds_read_b128 v[30:33], v30 offset:3072
	v_cndmask_b32_e32 v164, v184, v208, vcc
	v_lshl_add_u64 v[242:243], s[34:35], 0, v[164:165]
	s_mov_b32 m0, s41
	v_lshl_add_u64 v[242:243], v[242:243], 0, v[166:167]
	v_cndmask_b32_e32 v164, v182, v207, vcc
	ds_read_b128 v[210:213], v203 offset:32768
	ds_read_b128 v[214:217], v203 offset:33792
	ds_read_b128 v[218:221], v203 offset:34816
	ds_read_b128 v[222:225], v203 offset:35840
	ds_read_b128 v[226:229], v203 offset:36864
	ds_read_b128 v[230:233], v203 offset:37888
	ds_read_b128 v[234:237], v203 offset:38912
	ds_read_b128 v[238:241], v203 offset:39936
	global_load_lds_dwordx4 v[242:243], off
	v_lshl_add_u64 v[242:243], s[34:35], 0, v[164:165]
	v_lshl_add_u64 v[242:243], v[242:243], 0, v[166:167]
	s_mov_b32 m0, s42
	s_nop 0
	global_load_lds_dwordx4 v[242:243], off
	s_waitcnt vmcnt(8)
	s_waitcnt lgkmcnt(0)
	s_barrier
	s_setprio 1
	s_waitcnt lgkmcnt(0)
	v_mfma_f32_16x16x128_f8f6f4 v[158:161], v[2:9], v[210:217], v[158:161]
	v_mfma_f32_16x16x128_f8f6f4 v[150:153], v[10:17], v[210:217], v[150:153]
	v_mfma_f32_16x16x128_f8f6f4 v[142:145], v[2:9], v[218:225], v[142:145]
	v_mfma_f32_16x16x128_f8f6f4 v[134:137], v[10:17], v[218:225], v[134:137]
	v_mfma_f32_16x16x128_f8f6f4 v[126:129], v[2:9], v[226:233], v[126:129]
	v_mfma_f32_16x16x128_f8f6f4 v[118:121], v[10:17], v[226:233], v[118:121]
	v_mfma_f32_16x16x128_f8f6f4 v[110:113], v[2:9], v[234:241], v[110:113]
	v_mfma_f32_16x16x128_f8f6f4 v[102:105], v[10:17], v[234:241], v[102:105]
	s_setprio 0
	s_setprio 1
	v_mfma_f32_16x16x128_f8f6f4 v[154:157], v[18:25], v[210:217], v[154:157]
	v_mfma_f32_16x16x128_f8f6f4 v[146:149], v[26:33], v[210:217], v[146:149]
	v_mfma_f32_16x16x128_f8f6f4 v[138:141], v[18:25], v[218:225], v[138:141]
	v_mfma_f32_16x16x128_f8f6f4 v[130:133], v[26:33], v[218:225], v[130:133]
	v_mfma_f32_16x16x128_f8f6f4 v[122:125], v[18:25], v[226:233], v[122:125]
	v_mfma_f32_16x16x128_f8f6f4 v[114:117], v[26:33], v[226:233], v[114:117]
	v_mfma_f32_16x16x128_f8f6f4 v[106:109], v[18:25], v[234:241], v[106:109]
	v_mfma_f32_16x16x128_f8f6f4 v[98:101], v[26:33], v[234:241], v[98:101]
	s_setprio 0
	s_barrier
	s_add_i32 s30, s30, s38
	v_lshl_add_u64 v[190:191], v[190:191], 0, s[12:13]
	s_mov_b32 m0, s30
	ds_read_b128 v[210:213], v203 offset:49152
	ds_read_b128 v[214:217], v203 offset:50176
	ds_read_b128 v[218:221], v203 offset:51200
	ds_read_b128 v[222:225], v203 offset:52224
	ds_read_b128 v[226:229], v203 offset:53248
	ds_read_b128 v[230:233], v203 offset:54272
	ds_read_b128 v[234:237], v203 offset:55296
	ds_read_b128 v[238:241], v203 offset:56320
	global_load_lds_dwordx4 v[190:191], off
	s_add_i32 m0, s30, 0x2000
	s_add_u32 s28, s28, 0x40080
	v_lshl_add_u64 v[190:191], v[192:193], 0, s[12:13]
	s_addc_u32 s29, s29, 0
	s_add_i32 s30, s31, s38
	global_load_lds_dwordx4 v[190:191], off
	v_lshl_add_u64 v[190:191], s[28:29], 0, v[168:169]
	s_mov_b32 m0, s30
	s_nop 0
	global_load_lds_dwordx4 v[190:191], off
	v_lshl_add_u64 v[190:191], s[28:29], 0, v[172:173]
	s_add_i32 m0, s30, 0x2000
	s_nop 0
	global_load_lds_dwordx4 v[190:191], off
	v_lshl_add_u64 v[190:191], v[194:195], 0, s[12:13]
	s_mov_b32 m0, s46
	s_nop 0
	global_load_lds_dwordx4 v[190:191], off
	v_lshl_add_u64 v[190:191], v[196:197], 0, s[12:13]
	s_mov_b32 m0, s47
	s_nop 0
	global_load_lds_dwordx4 v[190:191], off
	s_waitcnt vmcnt(8)
	s_waitcnt lgkmcnt(0)
	s_barrier
	s_setprio 1
	s_waitcnt lgkmcnt(0)
	v_mfma_f32_16x16x128_f8f6f4 v[94:97], v[2:9], v[210:217], v[94:97]
	v_mfma_f32_16x16x128_f8f6f4 v[86:89], v[10:17], v[210:217], v[86:89]
	v_mfma_f32_16x16x128_f8f6f4 v[78:81], v[2:9], v[218:225], v[78:81]
	v_mfma_f32_16x16x128_f8f6f4 v[70:73], v[10:17], v[218:225], v[70:73]
	v_mfma_f32_16x16x128_f8f6f4 v[62:65], v[2:9], v[226:233], v[62:65]
	v_mfma_f32_16x16x128_f8f6f4 v[54:57], v[10:17], v[226:233], v[54:57]
	v_mfma_f32_16x16x128_f8f6f4 v[46:49], v[2:9], v[234:241], v[46:49]
	v_mfma_f32_16x16x128_f8f6f4 v[38:41], v[10:17], v[234:241], v[38:41]
	s_setprio 0
	s_setprio 1
	v_mfma_f32_16x16x128_f8f6f4 v[90:93], v[18:25], v[210:217], v[90:93]
	v_mfma_f32_16x16x128_f8f6f4 v[82:85], v[26:33], v[210:217], v[82:85]
	v_mfma_f32_16x16x128_f8f6f4 v[74:77], v[18:25], v[218:225], v[74:77]
	v_mfma_f32_16x16x128_f8f6f4 v[66:69], v[26:33], v[218:225], v[66:69]
	v_mfma_f32_16x16x128_f8f6f4 v[58:61], v[18:25], v[226:233], v[58:61]
	v_mfma_f32_16x16x128_f8f6f4 v[50:53], v[26:33], v[226:233], v[50:53]
	v_mfma_f32_16x16x128_f8f6f4 v[42:45], v[18:25], v[234:241], v[42:45]
	v_mfma_f32_16x16x128_f8f6f4 v[34:37], v[26:33], v[234:241], v[34:37]
	s_setprio 0
	s_add_i32 s62, s62, 2
	s_cmp_gt_u32 s62, 13
	s_mov_b64 s[30:31], s[26:27]
	s_barrier
	s_cbranch_scc0 .LBB0_1428
	s_nop 15
	s_nop 15
	s_and_b64 vcc, exec, s[14:15]
	s_cbranch_vccz .LBB0_1431
	s_barrier

; #define PG8_STAGE(bufoff, gbase, voff) do { _Pragma("unroll") for (int _i = 0; _i < 2; ++_i) \
;         __builtin_amdgcn_global_load_lds((const unsigned*)((const char*)(gbase) + (voff)[_i]), (LAS unsigned*)(lds + (bufoff) + ldsw + _i * 8192), 16, 0, 0); } while (0)
; #define PG8_LDA(dst, b, h) do { if constexpr (FP8) { _Pragma("unroll") for (int m = 0; m < 4; ++m) dst##8[m] = PG8_LD8(lds + PG8_SA(b, h) + aoff + m * 2048); } \
;         else { _Pragma("unroll") for (int m = 0; m < 4; ++m) _Pragma("unroll") for (int k = 0; k < 2; ++k) dst[m][k] = *(const LAS bf16x8*)(lds + PG8_SA(b, h) + aoff + m * 2048 + k * 1024); } } while (0)
; #define PG8_WAIT_V(n) asm volatile("s_waitcnt vmcnt(" #n ")" ::: "memory")
; #define PG8_WAIT_L(n) asm volatile("s_waitcnt lgkmcnt(" #n ")" ::: "memory")
; template <class Epi, class Sched, bool GATHER, bool FP8 = false>
; __device__ __forceinline__ void gemm_phase(LAS unsigned char* lds, const Gemm g, const Sched& S, const Epi& E) {
;     ...
;         for (int t = 0; t < nt; t += 2) {
;             const bool last = (t == nt - 2);
;             const char* a1 = cA + (size_t)(t + 1) * kstep;
;             const char* a2 = last ? nA : cA + (size_t)(t + 2) * kstep; const char* b2 = last ? nB : cB + (size_t)(t + 2) * kstep;
;             const char* a3 = a2 + kstep; const char* b3 = b2 + kstep;
;             PG8_LDB(B0, 0, 0); PG8_LDB(B1, 0, 1); PG8_SCHED; PG8_LDA(At, 0, 0); PG8_STAGE_A(PG8_SA(1, 1), a1, 1, false);
;             PG8_WAIT_V(8); PG8_WAIT_L(0); PG8_BAR; PG8_MMA(0, 0, At, B0); PG8_MMA(0, 1, At, B1); PG8_BAR; PG8_SCHED;
;             PG8_LDA(At, 0, 1); PG8_STAGE(PG8_SB(0, 0), b2, voffB); PG8_STAGE(PG8_SB(0, 1), b2 + hstep, voffB); PG8_STAGE_A(PG8_SA(0, 0), a2, 0, last);
;             PG8_WAIT_V(8); PG8_WAIT_L(0); PG8_BAR; PG8_MMA(1, 0, At, B0); PG8_MMA(1, 1, At, B1); PG8_BAR; PG8_SCHED;
;             PG8_LDB(B0, 1, 0); PG8_LDB(B1, 1, 1); PG8_SCHED; PG8_LDA(At, 1, 0); PG8_STAGE_A(PG8_SA(0, 1), a2, 1, last);
;             PG8_WAIT_V(8); PG8_WAIT_L(0); PG8_BAR; PG8_MMA(0, 0, At, B0); PG8_MMA(0, 1, At, B1); PG8_BAR; PG8_SCHED;
;             PG8_LDA(At, 1, 1); PG8_STAGE(PG8_SB(1, 0), b3, voffB); PG8_STAGE(PG8_SB(1, 1), b3 + hstep, voffB); PG8_STAGE_A(PG8_SA(1, 0), a3, 0, last);
;             PG8_WAIT_V(8); PG8_WAIT_L(0); PG8_BAR; PG8_MMA(1, 0, At, B0); PG8_MMA(1, 1, At, B1); PG8_BAR; PG8_SCHED;
.LBB0_1521:
	ds_read_b128 v[18:21], v190
	ds_read_b128 v[22:25], v190 offset:1024
	ds_read_b128 v[26:29], v190 offset:2048
	ds_read_b128 v[30:33], v190 offset:3072
	ds_read_b128 v[2:5], v191
	ds_read_b128 v[6:9], v191 offset:1024
	ds_read_b128 v[10:13], v191 offset:2048
	ds_read_b128 v[14:17], v191 offset:3072
	s_add_u32 s40, s6, 0xfffc0080
	s_addc_u32 s41, s7, -1
	s_cmp_eq_u32 s61, 12
	s_cselect_b32 s43, s23, s41
	s_cselect_b32 s42, s25, s40
	s_cselect_b32 s41, s29, s39
	s_cselect_b32 s40, s28, s27
	v_lshl_add_u64 v[218:219], s[6:7], 0, v[176:177]
	s_add_i32 m0, s35, 0xc000
	ds_read_b128 v[180:183], v192
	ds_read_b128 v[184:187], v192 offset:1024
	ds_read_b128 v[194:197], v192 offset:2048
	ds_read_b128 v[198:201], v192 offset:3072
	ds_read_b128 v[202:205], v192 offset:4096
	ds_read_b128 v[206:209], v192 offset:5120
	ds_read_b128 v[210:213], v192 offset:6144
	ds_read_b128 v[214:217], v192 offset:7168
	global_load_lds_dwordx4 v[218:219], off
	v_lshl_add_u64 v[218:219], s[6:7], 0, v[178:179]
	s_add_i32 m0, s35, 0xe000
	s_nop 0
	global_load_lds_dwordx4 v[218:219], off
	s_waitcnt vmcnt(8)
	s_waitcnt lgkmcnt(0)
	s_barrier
	s_setprio 1
	s_waitcnt lgkmcnt(0)
	v_mfma_f32_16x16x128_f8f6f4 v[158:161], v[18:25], v[180:187], v[158:161]
	v_mfma_f32_16x16x128_f8f6f4 v[154:157], v[26:33], v[180:187], v[154:157]
	v_mfma_f32_16x16x128_f8f6f4 v[142:145], v[18:25], v[194:201], v[142:145]
	v_mfma_f32_16x16x128_f8f6f4 v[138:141], v[26:33], v[194:201], v[138:141]
	v_mfma_f32_16x16x128_f8f6f4 v[126:129], v[18:25], v[202:209], v[126:129]
	v_mfma_f32_16x16x128_f8f6f4 v[122:125], v[26:33], v[202:209], v[122:125]
	v_mfma_f32_16x16x128_f8f6f4 v[110:113], v[18:25], v[210:217], v[110:113]
	v_mfma_f32_16x16x128_f8f6f4 v[106:109], v[26:33], v[210:217], v[106:109]
	s_setprio 0
	s_setprio 1
	v_mfma_f32_16x16x128_f8f6f4 v[150:153], v[2:9], v[180:187], v[150:153]
	v_mfma_f32_16x16x128_f8f6f4 v[146:149], v[10:17], v[180:187], v[146:149]
	v_mfma_f32_16x16x128_f8f6f4 v[134:137], v[2:9], v[194:201], v[134:137]
	v_mfma_f32_16x16x128_f8f6f4 v[130:133], v[10:17], v[194:201], v[130:133]
	v_mfma_f32_16x16x128_f8f6f4 v[118:121], v[2:9], v[202:209], v[118:121]
	v_mfma_f32_16x16x128_f8f6f4 v[114:117], v[10:17], v[202:209], v[114:117]
	v_mfma_f32_16x16x128_f8f6f4 v[102:105], v[2:9], v[210:217], v[102:105]
	v_mfma_f32_16x16x128_f8f6f4 v[98:101], v[10:17], v[210:217], v[98:101]
	s_setprio 0
	s_barrier
	s_add_i32 s62, s56, s47
	v_lshl_add_u64 v[180:181], s[40:41], 0, v[166:167]
	s_mov_b32 m0, s62
	ds_read_b128 v[194:197], v192 offset:16384
	ds_read_b128 v[198:201], v192 offset:17408
	ds_read_b128 v[202:205], v192 offset:18432
	ds_read_b128 v[206:209], v192 offset:19456
	ds_read_b128 v[210:213], v192 offset:20480
	ds_read_b128 v[214:217], v192 offset:21504
	ds_read_b128 v[218:221], v192 offset:22528
	ds_read_b128 v[222:225], v192 offset:23552
	global_load_lds_dwordx4 v[180:181], off
	s_add_i32 m0, s62, 0x2000
	s_add_u32 s62, s40, 0x40000
	v_lshl_add_u64 v[182:183], s[40:41], 0, v[172:173]
	s_addc_u32 s63, s41, 0
	s_add_i32 s64, s57, s47
	global_load_lds_dwordx4 v[182:183], off
	v_lshl_add_u64 v[184:185], s[62:63], 0, v[166:167]
	s_mov_b32 m0, s64
	v_lshl_add_u64 v[186:187], s[42:43], 0, v[168:169]
	global_load_lds_dwordx4 v[184:185], off
	v_lshl_add_u64 v[184:185], s[62:63], 0, v[172:173]
	s_add_i32 m0, s64, 0x2000
	s_nop 0
	global_load_lds_dwordx4 v[184:185], off
	v_lshl_add_u64 v[184:185], s[42:43], 0, v[164:165]
	s_mov_b32 m0, s35
	s_nop 0
	global_load_lds_dwordx4 v[184:185], off
	s_mov_b32 m0, s37
	s_nop 0
	global_load_lds_dwordx4 v[186:187], off
	s_waitcnt vmcnt(8)
	s_waitcnt lgkmcnt(0)
	s_barrier
	s_setprio 1
	s_waitcnt lgkmcnt(0)
	v_mfma_f32_16x16x128_f8f6f4 v[94:97], v[18:25], v[194:201], v[94:97]
	v_mfma_f32_16x16x128_f8f6f4 v[90:93], v[26:33], v[194:201], v[90:93]
	v_mfma_f32_16x16x128_f8f6f4 v[78:81], v[18:25], v[202:209], v[78:81]
	v_mfma_f32_16x16x128_f8f6f4 v[74:77], v[26:33], v[202:209], v[74:77]
	v_mfma_f32_16x16x128_f8f6f4 v[62:65], v[18:25], v[210:217], v[62:65]
	v_mfma_f32_16x16x128_f8f6f4 v[58:61], v[26:33], v[210:217], v[58:61]
	v_mfma_f32_16x16x128_f8f6f4 v[46:49], v[18:25], v[218:225], v[46:49]
	v_mfma_f32_16x16x128_f8f6f4 v[42:45], v[26:33], v[218:225], v[42:45]
	s_setprio 0
	s_setprio 1
	v_mfma_f32_16x16x128_f8f6f4 v[86:89], v[2:9], v[194:201], v[86:89]
	v_mfma_f32_16x16x128_f8f6f4 v[82:85], v[10:17], v[194:201], v[82:85]
	v_mfma_f32_16x16x128_f8f6f4 v[70:73], v[2:9], v[202:209], v[70:73]
	v_mfma_f32_16x16x128_f8f6f4 v[66:69], v[10:17], v[202:209], v[66:69]
	v_mfma_f32_16x16x128_f8f6f4 v[54:57], v[2:9], v[210:217], v[54:57]
	v_mfma_f32_16x16x128_f8f6f4 v[50:53], v[10:17], v[210:217], v[50:53]
	v_mfma_f32_16x16x128_f8f6f4 v[38:41], v[2:9], v[218:225], v[38:41]
	v_mfma_f32_16x16x128_f8f6f4 v[34:37], v[10:17], v[218:225], v[34:37]
	s_setprio 0
	s_barrier
; #define PG8_STAGE(bufoff, gbase, voff) do { _Pragma("unroll") for (int _i = 0; _i < 2; ++_i) \
;         __builtin_amdgcn_global_load_lds((const unsigned*)((const char*)(gbase) + (voff)[_i]), (LAS unsigned*)(lds + (bufoff) + ldsw + _i * 8192), 16, 0, 0); } while (0)
; #define PG8_LDA(dst, b, h) do { if constexpr (FP8) { _Pragma("unroll") for (int m = 0; m < 4; ++m) dst##8[m] = PG8_LD8(lds + PG8_SA(b, h) + aoff + m * 2048); } \
;         else { _Pragma("unroll") for (int m = 0; m < 4; ++m) _Pragma("unroll") for (int k = 0; k < 2; ++k) dst[m][k] = *(const LAS bf16x8*)(lds + PG8_SA(b, h) + aoff + m * 2048 + k * 1024); } } while (0)
; #define PG8_WAIT_V(n) asm volatile("s_waitcnt vmcnt(" #n ")" ::: "memory")
; #define PG8_WAIT_L(n) asm volatile("s_waitcnt lgkmcnt(" #n ")" ::: "memory")
; template <class Epi, class Sched, bool GATHER, bool FP8 = false>
; __device__ __forceinline__ void gemm_phase(LAS unsigned char* lds, const Gemm g, const Sched& S, const Epi& E) {
;     ...
;         for (int t = 0; t < nt; t += 2) {
;             const bool last = (t == nt - 2);
;             const char* a1 = cA + (size_t)(t + 1) * kstep;
;             const char* a2 = last ? nA : cA + (size_t)(t + 2) * kstep; const char* b2 = last ? nB : cB + (size_t)(t + 2) * kstep;
;             const char* a3 = a2 + kstep; const char* b3 = b2 + kstep;
;             PG8_LDB(B0, 0, 0); PG8_LDB(B1, 0, 1); PG8_SCHED; PG8_LDA(At, 0, 0); PG8_STAGE_A(PG8_SA(1, 1), a1, 1, false);
;             PG8_WAIT_V(8); PG8_WAIT_L(0); PG8_BAR; PG8_MMA(0, 0, At, B0); PG8_MMA(0, 1, At, B1); PG8_BAR; PG8_SCHED;
;             PG8_LDA(At, 0, 1); PG8_STAGE(PG8_SB(0, 0), b2, voffB); PG8_STAGE(PG8_SB(0, 1), b2 + hstep, voffB); PG8_STAGE_A(PG8_SA(0, 0), a2, 0, last);
;             PG8_WAIT_V(8); PG8_WAIT_L(0); PG8_BAR; PG8_MMA(1, 0, At, B0); PG8_MMA(1, 1, At, B1); PG8_BAR; PG8_SCHED;
;             PG8_LDB(B0, 1, 0); PG8_LDB(B1, 1, 1); PG8_SCHED; PG8_LDA(At, 1, 0); PG8_STAGE_A(PG8_SA(0, 1), a2, 1, last);
;             PG8_WAIT_V(8); PG8_WAIT_L(0); PG8_BAR; PG8_MMA(0, 0, At, B0); PG8_MMA(0, 1, At, B1); PG8_BAR; PG8_SCHED;
;             PG8_LDA(At, 1, 1); PG8_STAGE(PG8_SB(1, 0), b3, voffB); PG8_STAGE(PG8_SB(1, 1), b3 + hstep, voffB); PG8_STAGE_A(PG8_SA(1, 0), a3, 0, last);
;             PG8_WAIT_V(8); PG8_WAIT_L(0); PG8_BAR; PG8_MMA(1, 0, At, B0); PG8_MMA(1, 1, At, B1); PG8_BAR; PG8_SCHED;
	s_add_i32 s62, 0, 0x18000
	s_add_i32 s63, 0, 0x1c000
	v_add_u32_e32 v14, s62, v189
	v_add_u32_e32 v30, s63, v189
	ds_read_b128 v[2:5], v14
	ds_read_b128 v[6:9], v14 offset:1024
	ds_read_b128 v[10:13], v14 offset:2048
	ds_read_b128 v[14:17], v14 offset:3072
	ds_read_b128 v[18:21], v30
	ds_read_b128 v[22:25], v30 offset:1024
	ds_read_b128 v[26:29], v30 offset:2048
	ds_read_b128 v[30:33], v30 offset:3072
	s_add_u32 s42, s42, 0x40000
	s_addc_u32 s43, s43, 0
	s_mov_b32 m0, s48
	v_lshl_add_u64 v[226:227], s[42:43], 0, v[164:165]
	ds_read_b128 v[194:197], v192 offset:32768
	ds_read_b128 v[198:201], v192 offset:33792
	ds_read_b128 v[202:205], v192 offset:34816
	ds_read_b128 v[206:209], v192 offset:35840
	ds_read_b128 v[210:213], v192 offset:36864
	ds_read_b128 v[214:217], v192 offset:37888
	ds_read_b128 v[218:221], v192 offset:38912
	ds_read_b128 v[222:225], v192 offset:39936
	global_load_lds_dwordx4 v[226:227], off
	v_lshl_add_u64 v[226:227], s[42:43], 0, v[168:169]
	s_mov_b32 m0, s49
	s_nop 0
	global_load_lds_dwordx4 v[226:227], off
	s_waitcnt vmcnt(8)
	s_waitcnt lgkmcnt(0)
	s_barrier
	s_setprio 1
	s_waitcnt lgkmcnt(0)
	v_mfma_f32_16x16x128_f8f6f4 v[158:161], v[2:9], v[194:201], v[158:161]
	v_mfma_f32_16x16x128_f8f6f4 v[154:157], v[10:17], v[194:201], v[154:157]
	v_mfma_f32_16x16x128_f8f6f4 v[142:145], v[2:9], v[202:209], v[142:145]
	v_mfma_f32_16x16x128_f8f6f4 v[138:141], v[10:17], v[202:209], v[138:141]
	v_mfma_f32_16x16x128_f8f6f4 v[126:129], v[2:9], v[210:217], v[126:129]
	v_mfma_f32_16x16x128_f8f6f4 v[122:125], v[10:17], v[210:217], v[122:125]
	v_mfma_f32_16x16x128_f8f6f4 v[110:113], v[2:9], v[218:225], v[110:113]
	v_mfma_f32_16x16x128_f8f6f4 v[106:109], v[10:17], v[218:225], v[106:109]
	s_setprio 0
	s_setprio 1
	v_mfma_f32_16x16x128_f8f6f4 v[150:153], v[18:25], v[194:201], v[150:153]
	v_mfma_f32_16x16x128_f8f6f4 v[146:149], v[26:33], v[194:201], v[146:149]
	v_mfma_f32_16x16x128_f8f6f4 v[134:137], v[18:25], v[202:209], v[134:137]
	v_mfma_f32_16x16x128_f8f6f4 v[130:133], v[26:33], v[202:209], v[130:133]
	v_mfma_f32_16x16x128_f8f6f4 v[118:121], v[18:25], v[210:217], v[118:121]
	v_mfma_f32_16x16x128_f8f6f4 v[114:117], v[26:33], v[210:217], v[114:117]
	v_mfma_f32_16x16x128_f8f6f4 v[102:105], v[18:25], v[218:225], v[102:105]
	v_mfma_f32_16x16x128_f8f6f4 v[98:101], v[26:33], v[218:225], v[98:101]
	s_setprio 0
	s_barrier
	s_add_i32 s42, s62, s47
	v_lshl_add_u64 v[180:181], v[180:181], 0, s[14:15]
	s_mov_b32 m0, s42
	ds_read_b128 v[194:197], v192 offset:49152
	ds_read_b128 v[198:201], v192 offset:50176
	ds_read_b128 v[202:205], v192 offset:51200
	ds_read_b128 v[206:209], v192 offset:52224
	ds_read_b128 v[210:213], v192 offset:53248
	ds_read_b128 v[214:217], v192 offset:54272
	ds_read_b128 v[218:221], v192 offset:55296
	ds_read_b128 v[222:225], v192 offset:56320
	global_load_lds_dwordx4 v[180:181], off
	s_add_i32 m0, s42, 0x2000
	s_add_u32 s40, s40, 0x40080
	v_lshl_add_u64 v[180:181], v[182:183], 0, s[14:15]
	s_addc_u32 s41, s41, 0
	s_add_i32 s42, s63, s47
	global_load_lds_dwordx4 v[180:181], off
	v_lshl_add_u64 v[180:181], s[40:41], 0, v[166:167]
	s_mov_b32 m0, s42
	s_nop 0
	global_load_lds_dwordx4 v[180:181], off
	v_lshl_add_u64 v[180:181], s[40:41], 0, v[172:173]
	s_add_i32 m0, s42, 0x2000
	s_nop 0
	global_load_lds_dwordx4 v[180:181], off
	v_lshl_add_u64 v[180:181], v[184:185], 0, s[14:15]
	s_mov_b32 m0, s52
	s_nop 0
	global_load_lds_dwordx4 v[180:181], off
	v_lshl_add_u64 v[180:181], v[186:187], 0, s[14:15]
	s_mov_b32 m0, s53
	s_nop 0
	global_load_lds_dwordx4 v[180:181], off
	s_waitcnt vmcnt(8)
	s_waitcnt lgkmcnt(0)
	s_barrier
	s_setprio 1
	s_waitcnt lgkmcnt(0)
	v_mfma_f32_16x16x128_f8f6f4 v[94:97], v[2:9], v[194:201], v[94:97]
	v_mfma_f32_16x16x128_f8f6f4 v[90:93], v[10:17], v[194:201], v[90:93]
	v_mfma_f32_16x16x128_f8f6f4 v[78:81], v[2:9], v[202:209], v[78:81]
	v_mfma_f32_16x16x128_f8f6f4 v[74:77], v[10:17], v[202:209], v[74:77]
	v_mfma_f32_16x16x128_f8f6f4 v[62:65], v[2:9], v[210:217], v[62:65]
	v_mfma_f32_16x16x128_f8f6f4 v[58:61], v[10:17], v[210:217], v[58:61]
	v_mfma_f32_16x16x128_f8f6f4 v[46:49], v[2:9], v[218:225], v[46:49]
	v_mfma_f32_16x16x128_f8f6f4 v[42:45], v[10:17], v[218:225], v[42:45]
	s_setprio 0
	s_setprio 1
	v_mfma_f32_16x16x128_f8f6f4 v[86:89], v[18:25], v[194:201], v[86:89]
	v_mfma_f32_16x16x128_f8f6f4 v[82:85], v[26:33], v[194:201], v[82:85]
	v_mfma_f32_16x16x128_f8f6f4 v[70:73], v[18:25], v[202:209], v[70:73]
	v_mfma_f32_16x16x128_f8f6f4 v[66:69], v[26:33], v[202:209], v[66:69]
	v_mfma_f32_16x16x128_f8f6f4 v[54:57], v[18:25], v[210:217], v[54:57]
	v_mfma_f32_16x16x128_f8f6f4 v[50:53], v[26:33], v[210:217], v[50:53]
	v_mfma_f32_16x16x128_f8f6f4 v[38:41], v[18:25], v[218:225], v[38:41]
	v_mfma_f32_16x16x128_f8f6f4 v[34:37], v[26:33], v[218:225], v[34:37]
	s_setprio 0
	s_add_i32 s61, s61, 2
	s_add_u32 s6, s6, 0x100
	s_addc_u32 s7, s7, 0
	s_add_u32 s27, s27, 0x100
	s_addc_u32 s39, s39, 0
	s_cmp_gt_u32 s61, 13
	s_barrier
	s_cbranch_scc0 .LBB0_1521
	s_nop 15
	s_nop 15
	s_and_b64 vcc, exec, s[16:17]
	s_cbranch_vccz .LBB0_1524
	s_barrier
